# prep phase modulation tiles: the 20 serial staging loads issued together; GEMV batches software-pipelined (two 32-load batches in flight)
# baseline (speedup 1.0000x reference)
; __device__ __forceinline__ float silu_f(float x) { return x * __builtin_amdgcn_rcpf(1.f + __expf(-x)); }
; __device__ __forceinline__ void ph_prep(Ctx& c, int gtid, int gthreads, int bid, int G, float* lds) {
;     ...
;     for (int tile = bid; tile < 192; tile += G) {
;         const int l = tile / 96, j0 = (tile % 96) * 64;
;         __syncthreads();
;         for (int idx = tid; idx < 5 * D; idx += NTHR) { const int r = idx >> 10, k = idx & 1023; lds[idx] = silu_f(r < 4 ? c.in(1)[r * D + k] : c.in(3)[k]); }
;         __syncthreads();
.LBB0_594:
	s_barrier
	s_and_saveexec_b64 s[28:29], s[0:1]
	s_cbranch_execz .LBB0_601
	s_load_dwordx2 s[16:17], s[4:5], 0x8
	s_load_dwordx2 s[44:45], s[4:5], 0x18
	v_add_u32_e32 v105, 0x1000, v22
	v_add_u32_e32 v106, 0x2000, v22
	v_add_u32_e32 v107, 0x3000, v22
	s_waitcnt lgkmcnt(0)
	global_load_dword v160, v22, s[16:17]
	global_load_dword v161, v22, s[16:17] offset:1024
	global_load_dword v162, v22, s[16:17] offset:2048
	global_load_dword v163, v22, s[16:17] offset:3072
	global_load_dword v164, v105, s[16:17]
	global_load_dword v165, v105, s[16:17] offset:1024
	global_load_dword v166, v105, s[16:17] offset:2048
	global_load_dword v167, v105, s[16:17] offset:3072
	global_load_dword v168, v106, s[16:17]
	global_load_dword v169, v106, s[16:17] offset:1024
	global_load_dword v170, v106, s[16:17] offset:2048
	global_load_dword v171, v106, s[16:17] offset:3072
	global_load_dword v172, v107, s[16:17]
	global_load_dword v173, v107, s[16:17] offset:1024
	global_load_dword v174, v107, s[16:17] offset:2048
	global_load_dword v175, v107, s[16:17] offset:3072
	global_load_dword v176, v22, s[44:45]
	global_load_dword v177, v22, s[44:45] offset:1024
	global_load_dword v178, v22, s[44:45] offset:2048
	global_load_dword v179, v22, s[44:45] offset:3072
	s_waitcnt vmcnt(19)
	v_mul_f32_e32 v108, 0xbfb8aa3b, v160
	v_exp_f32_e32 v108, v108
	s_nop 0
	v_add_f32_e32 v108, 1.0, v108
	v_rcp_f32_e32 v108, v108
	s_nop 0
	v_mul_f32_e32 v109, v160, v108
	ds_write_b32 v29, v109
	s_waitcnt vmcnt(18)
	v_mul_f32_e32 v108, 0xbfb8aa3b, v161
	v_exp_f32_e32 v108, v108
	s_nop 0
	v_add_f32_e32 v108, 1.0, v108
	v_rcp_f32_e32 v108, v108
	s_nop 0
	v_mul_f32_e32 v109, v161, v108
	ds_write_b32 v29, v109 offset:1024
	s_waitcnt vmcnt(17)
	v_mul_f32_e32 v108, 0xbfb8aa3b, v162
	v_exp_f32_e32 v108, v108
	s_nop 0
	v_add_f32_e32 v108, 1.0, v108
	v_rcp_f32_e32 v108, v108
	s_nop 0
	v_mul_f32_e32 v109, v162, v108
	ds_write_b32 v29, v109 offset:2048
	s_waitcnt vmcnt(16)
	v_mul_f32_e32 v108, 0xbfb8aa3b, v163
	v_exp_f32_e32 v108, v108
	s_nop 0
	v_add_f32_e32 v108, 1.0, v108
	v_rcp_f32_e32 v108, v108
	s_nop 0
	v_mul_f32_e32 v109, v163, v108
	ds_write_b32 v29, v109 offset:3072
	s_waitcnt vmcnt(15)
	v_mul_f32_e32 v108, 0xbfb8aa3b, v164
	v_exp_f32_e32 v108, v108
	s_nop 0
	v_add_f32_e32 v108, 1.0, v108
	v_rcp_f32_e32 v108, v108
	s_nop 0
	v_mul_f32_e32 v109, v164, v108
	ds_write_b32 v29, v109 offset:4096
	s_waitcnt vmcnt(14)
	v_mul_f32_e32 v108, 0xbfb8aa3b, v165
	v_exp_f32_e32 v108, v108
	s_nop 0
	v_add_f32_e32 v108, 1.0, v108
	v_rcp_f32_e32 v108, v108
	s_nop 0
	v_mul_f32_e32 v109, v165, v108
	ds_write_b32 v29, v109 offset:5120
	s_waitcnt vmcnt(13)
	v_mul_f32_e32 v108, 0xbfb8aa3b, v166
	v_exp_f32_e32 v108, v108
	s_nop 0
	v_add_f32_e32 v108, 1.0, v108
	v_rcp_f32_e32 v108, v108
	s_nop 0
	v_mul_f32_e32 v109, v166, v108
	ds_write_b32 v29, v109 offset:6144
	s_waitcnt vmcnt(12)
	v_mul_f32_e32 v108, 0xbfb8aa3b, v167
	v_exp_f32_e32 v108, v108
	s_nop 0
	v_add_f32_e32 v108, 1.0, v108
	v_rcp_f32_e32 v108, v108
	s_nop 0
	v_mul_f32_e32 v109, v167, v108
	ds_write_b32 v29, v109 offset:7168
	s_waitcnt vmcnt(11)
	v_mul_f32_e32 v108, 0xbfb8aa3b, v168
	v_exp_f32_e32 v108, v108
	s_nop 0
	v_add_f32_e32 v108, 1.0, v108
	v_rcp_f32_e32 v108, v108
	s_nop 0
	v_mul_f32_e32 v109, v168, v108
	ds_write_b32 v29, v109 offset:8192
	s_waitcnt vmcnt(10)
	v_mul_f32_e32 v108, 0xbfb8aa3b, v169
	v_exp_f32_e32 v108, v108
	s_nop 0
	v_add_f32_e32 v108, 1.0, v108
	v_rcp_f32_e32 v108, v108
	s_nop 0
	v_mul_f32_e32 v109, v169, v108
	ds_write_b32 v29, v109 offset:9216
	s_waitcnt vmcnt(9)
	v_mul_f32_e32 v108, 0xbfb8aa3b, v170
	v_exp_f32_e32 v108, v108
	s_nop 0
	v_add_f32_e32 v108, 1.0, v108
	v_rcp_f32_e32 v108, v108
	s_nop 0
	v_mul_f32_e32 v109, v170, v108
	ds_write_b32 v29, v109 offset:10240
	s_waitcnt vmcnt(8)
	v_mul_f32_e32 v108, 0xbfb8aa3b, v171
	v_exp_f32_e32 v108, v108
	s_nop 0
	v_add_f32_e32 v108, 1.0, v108
	v_rcp_f32_e32 v108, v108
	s_nop 0
	v_mul_f32_e32 v109, v171, v108
	ds_write_b32 v29, v109 offset:11264
	s_waitcnt vmcnt(7)
	v_mul_f32_e32 v108, 0xbfb8aa3b, v172
	v_exp_f32_e32 v108, v108
	s_nop 0
	v_add_f32_e32 v108, 1.0, v108
	v_rcp_f32_e32 v108, v108
	s_nop 0
	v_mul_f32_e32 v109, v172, v108
	ds_write_b32 v29, v109 offset:12288
	s_waitcnt vmcnt(6)
	v_mul_f32_e32 v108, 0xbfb8aa3b, v173
	v_exp_f32_e32 v108, v108
	s_nop 0
	v_add_f32_e32 v108, 1.0, v108
	v_rcp_f32_e32 v108, v108
	s_nop 0
	v_mul_f32_e32 v109, v173, v108
	ds_write_b32 v29, v109 offset:13312
	s_waitcnt vmcnt(5)
	v_mul_f32_e32 v108, 0xbfb8aa3b, v174
	v_exp_f32_e32 v108, v108
	s_nop 0
	v_add_f32_e32 v108, 1.0, v108
	v_rcp_f32_e32 v108, v108
	s_nop 0
	v_mul_f32_e32 v109, v174, v108
	ds_write_b32 v29, v109 offset:14336
	s_waitcnt vmcnt(4)
	v_mul_f32_e32 v108, 0xbfb8aa3b, v175
	v_exp_f32_e32 v108, v108
	s_nop 0
	v_add_f32_e32 v108, 1.0, v108
	v_rcp_f32_e32 v108, v108
	s_nop 0
	v_mul_f32_e32 v109, v175, v108
	ds_write_b32 v29, v109 offset:15360
	s_waitcnt vmcnt(3)
	v_mul_f32_e32 v108, 0xbfb8aa3b, v176
	v_exp_f32_e32 v108, v108
	s_nop 0
	v_add_f32_e32 v108, 1.0, v108
	v_rcp_f32_e32 v108, v108
	s_nop 0
	v_mul_f32_e32 v109, v176, v108
	ds_write_b32 v29, v109 offset:16384
	s_waitcnt vmcnt(2)
	v_mul_f32_e32 v108, 0xbfb8aa3b, v177
	v_exp_f32_e32 v108, v108
	s_nop 0
	v_add_f32_e32 v108, 1.0, v108
	v_rcp_f32_e32 v108, v108
	s_nop 0
	v_mul_f32_e32 v109, v177, v108
	ds_write_b32 v29, v109 offset:17408
	s_waitcnt vmcnt(1)
	v_mul_f32_e32 v108, 0xbfb8aa3b, v178
	v_exp_f32_e32 v108, v108
	s_nop 0
	v_add_f32_e32 v108, 1.0, v108
	v_rcp_f32_e32 v108, v108
	s_nop 0
	v_mul_f32_e32 v109, v178, v108
	ds_write_b32 v29, v109 offset:18432
	s_waitcnt vmcnt(0)
	v_mul_f32_e32 v108, 0xbfb8aa3b, v179
	v_exp_f32_e32 v108, v108
	s_nop 0
	v_add_f32_e32 v108, 1.0, v108
	v_rcp_f32_e32 v108, v108
	s_nop 0
	v_mul_f32_e32 v109, v179, v108
	ds_write_b32 v29, v109 offset:19456

;     template <class T> __device__ __forceinline__ T* w(size_t off) const { return (T*)(p->ws + off); }
; __device__ __forceinline__ void ph_prep(Ctx& c, int gtid, int gthreads, int bid, int G, float* lds) {
;     ...
;         const float* aw = c.in(4) + (size_t)l * D * 6144 + j0 + jj;
;         float acc[5] = {0.f, 0.f, 0.f, 0.f, 0.f};
;         for (int k0 = kq * 256; k0 < kq * 256 + 256; k0 += 32) {
;             float w[32];
; #pragma unroll
;             for (int i = 0; i < 32; ++i) w[i] = aw[(size_t)(k0 + i) * 6144];
; #pragma unroll
;             for (int i = 0; i < 32; ++i)
; #pragma unroll
;                 for (int r = 0; r < 5; ++r) acc[r] = fmaf(lds[r * D + k0 + i], w[i], acc[r]);
;         }
.Lmod_pre:
	s_mov_b64 s[16:17], 0xc0000
	v_add_co_u32_e32 v4, vcc, 0xfff46000, v26
	s_mov_b32 s7, 0xfffdc000
	s_nop 0
	v_addc_co_u32_e32 v5, vcc, -1, v27, vcc
	global_load_dword v82, v[4:5], off
	v_add_co_u32_e32 v4, vcc, 0xfff4c000, v26
	s_nop 0
	s_nop 0
	v_addc_co_u32_e32 v5, vcc, -1, v27, vcc
	global_load_dword v84, v[4:5], off
	v_add_co_u32_e32 v4, vcc, 0xfff52000, v26
	s_nop 0
	s_nop 0
	v_addc_co_u32_e32 v5, vcc, -1, v27, vcc
	global_load_dword v86, v[4:5], off
	v_add_co_u32_e32 v4, vcc, 0xfff58000, v26
	s_nop 1
	v_addc_co_u32_e32 v5, vcc, -1, v27, vcc
	global_load_dword v88, v[4:5], off
	v_add_co_u32_e32 v4, vcc, 0xfff5e000, v26
	s_nop 1
	v_addc_co_u32_e32 v5, vcc, -1, v27, vcc
	global_load_dword v74, v[4:5], off
	v_add_co_u32_e32 v4, vcc, 0xfff64000, v26
	s_nop 1
	v_addc_co_u32_e32 v5, vcc, -1, v27, vcc
	global_load_dword v76, v[4:5], off
	v_add_co_u32_e32 v4, vcc, 0xfff6a000, v26
	s_nop 1
	v_addc_co_u32_e32 v5, vcc, -1, v27, vcc
	global_load_dword v78, v[4:5], off
	v_add_co_u32_e32 v4, vcc, 0xfff70000, v26
	s_nop 1
	v_addc_co_u32_e32 v5, vcc, -1, v27, vcc
	global_load_dword v80, v[4:5], off
	v_add_co_u32_e32 v4, vcc, 0xfff76000, v26
	s_nop 1
	v_addc_co_u32_e32 v5, vcc, -1, v27, vcc
	global_load_dword v70, v[4:5], off
	v_add_co_u32_e32 v4, vcc, 0xfff7c000, v26
	s_nop 1
	v_addc_co_u32_e32 v5, vcc, -1, v27, vcc
	global_load_dword v72, v[4:5], off
	v_add_co_u32_e32 v4, vcc, 0xfff82000, v26
	s_nop 1
	v_addc_co_u32_e32 v5, vcc, -1, v27, vcc
	global_load_dword v66, v[4:5], off
	v_add_co_u32_e32 v4, vcc, 0xfff88000, v26
	s_nop 1
	v_addc_co_u32_e32 v5, vcc, -1, v27, vcc
	global_load_dword v68, v[4:5], off
	v_add_co_u32_e32 v4, vcc, 0xfff8e000, v26
	s_nop 1
	v_addc_co_u32_e32 v5, vcc, -1, v27, vcc
	global_load_dword v56, v[4:5], off
	v_add_co_u32_e32 v4, vcc, 0xfff94000, v26
	s_nop 1
	v_addc_co_u32_e32 v5, vcc, -1, v27, vcc
	global_load_dword v58, v[4:5], off
	v_add_co_u32_e32 v4, vcc, 0xfff9a000, v26
	s_nop 1
	v_addc_co_u32_e32 v5, vcc, -1, v27, vcc
	global_load_dword v60, v[4:5], off
	v_add_co_u32_e32 v4, vcc, 0xfffa0000, v26
	s_nop 1
	v_addc_co_u32_e32 v5, vcc, -1, v27, vcc
	global_load_dword v62, v[4:5], off
	v_add_co_u32_e32 v4, vcc, 0xfffa6000, v26
	s_nop 1
	v_addc_co_u32_e32 v5, vcc, -1, v27, vcc
	global_load_dword v48, v[4:5], off
	v_add_co_u32_e32 v4, vcc, 0xfffac000, v26
	s_nop 1
	v_addc_co_u32_e32 v5, vcc, -1, v27, vcc
	global_load_dword v50, v[4:5], off
	v_add_co_u32_e32 v4, vcc, 0xfffb2000, v26
	s_nop 1
	v_addc_co_u32_e32 v5, vcc, -1, v27, vcc
	global_load_dword v52, v[4:5], off
	v_add_co_u32_e32 v4, vcc, 0xfffb8000, v26
	s_nop 1
	v_addc_co_u32_e32 v5, vcc, -1, v27, vcc
	global_load_dword v54, v[4:5], off
	v_add_co_u32_e32 v4, vcc, 0xfffbe000, v26
	s_nop 1
	v_addc_co_u32_e32 v5, vcc, -1, v27, vcc
	global_load_dword v46, v[4:5], off
	v_add_co_u32_e32 v4, vcc, 0xfffc4000, v26
	s_nop 1
	v_addc_co_u32_e32 v5, vcc, -1, v27, vcc
	global_load_dword v2, v[4:5], off
	v_add_co_u32_e32 v4, vcc, 0xfffca000, v26
	s_nop 1
	v_addc_co_u32_e32 v5, vcc, -1, v27, vcc
	global_load_dword v30, v[4:5], off
	v_add_co_u32_e32 v4, vcc, 0xfffd0000, v26
	s_nop 1
	v_addc_co_u32_e32 v5, vcc, -1, v27, vcc
	global_load_dword v28, v[4:5], off
	v_add_co_u32_e32 v4, vcc, 0xfffd6000, v26
	s_nop 1
	v_addc_co_u32_e32 v5, vcc, -1, v27, vcc
	global_load_dword v32, v[4:5], off
	v_add_co_u32_e32 v4, vcc, s7, v26
	s_nop 1
	v_addc_co_u32_e32 v5, vcc, -1, v27, vcc
	global_load_dword v36, v[4:5], off
	v_add_co_u32_e32 v4, vcc, 0xfffe2000, v26
	s_nop 1
	v_addc_co_u32_e32 v5, vcc, -1, v27, vcc
	global_load_dword v40, v[4:5], off
	v_add_co_u32_e32 v4, vcc, 0xfffe8000, v26
	s_nop 1
	v_addc_co_u32_e32 v5, vcc, -1, v27, vcc
	global_load_dword v38, v[4:5], off
	v_add_co_u32_e32 v4, vcc, 0xfffee000, v26
	s_nop 1
	v_addc_co_u32_e32 v5, vcc, -1, v27, vcc
	global_load_dword v42, v[4:5], off
	v_add_co_u32_e32 v4, vcc, 0xffff4000, v26
	s_nop 1
	v_addc_co_u32_e32 v5, vcc, -1, v27, vcc
	global_load_dword v44, v[4:5], off
	v_add_co_u32_e32 v4, vcc, 0xffffa000, v26
	s_nop 1
	v_addc_co_u32_e32 v5, vcc, -1, v27, vcc
	global_load_dword v34, v[4:5], off
	global_load_dword v64, v[26:27], off
	v_lshl_add_u64 v[26:27], v[26:27], 0, s[16:17]
	s_mov_b32 s98, 0
.LBB0_602:
	v_add_co_u32_e32 v4, vcc, 0xfff46000, v26
	s_mov_b32 s7, 0xfffdc000
	s_nop 0
	v_addc_co_u32_e32 v5, vcc, -1, v27, vcc
	global_load_dword v104, v[4:5], off
	v_add_co_u32_e32 v4, vcc, 0xfff4c000, v26
	s_nop 0
	s_nop 0
	v_addc_co_u32_e32 v5, vcc, -1, v27, vcc
	global_load_dword v106, v[4:5], off
	v_add_co_u32_e32 v4, vcc, 0xfff52000, v26
	s_nop 0
	s_nop 0
	v_addc_co_u32_e32 v5, vcc, -1, v27, vcc
	global_load_dword v108, v[4:5], off
	v_add_co_u32_e32 v4, vcc, 0xfff58000, v26
	s_nop 1
	v_addc_co_u32_e32 v5, vcc, -1, v27, vcc
	global_load_dword v110, v[4:5], off
	v_add_co_u32_e32 v4, vcc, 0xfff5e000, v26
	s_nop 1
	v_addc_co_u32_e32 v5, vcc, -1, v27, vcc
	global_load_dword v112, v[4:5], off
	v_add_co_u32_e32 v4, vcc, 0xfff64000, v26
	s_nop 1
	v_addc_co_u32_e32 v5, vcc, -1, v27, vcc
	global_load_dword v114, v[4:5], off
	v_add_co_u32_e32 v4, vcc, 0xfff6a000, v26
	s_nop 1
	v_addc_co_u32_e32 v5, vcc, -1, v27, vcc
	global_load_dword v116, v[4:5], off
	v_add_co_u32_e32 v4, vcc, 0xfff70000, v26
	s_nop 1
	v_addc_co_u32_e32 v5, vcc, -1, v27, vcc
	global_load_dword v118, v[4:5], off
	v_add_co_u32_e32 v4, vcc, 0xfff76000, v26
	s_nop 1
	v_addc_co_u32_e32 v5, vcc, -1, v27, vcc
	global_load_dword v120, v[4:5], off
	v_add_co_u32_e32 v4, vcc, 0xfff7c000, v26
	s_nop 1
	v_addc_co_u32_e32 v5, vcc, -1, v27, vcc
	global_load_dword v122, v[4:5], off
	v_add_co_u32_e32 v4, vcc, 0xfff82000, v26
	s_nop 1
	v_addc_co_u32_e32 v5, vcc, -1, v27, vcc
;     template <class T> __device__ __forceinline__ T* w(size_t off) const { return (T*)(p->ws + off); }
; __device__ __forceinline__ void ph_prep(Ctx& c, int gtid, int gthreads, int bid, int G, float* lds) {
;     ...
;         for (int k0 = kq * 256; k0 < kq * 256 + 256; k0 += 32) {
;             float w[32];
; #pragma unroll
;             for (int i = 0; i < 32; ++i) w[i] = aw[(size_t)(k0 + i) * 6144];
; #pragma unroll
;             for (int i = 0; i < 32; ++i)
; #pragma unroll
;                 for (int r = 0; r < 5; ++r) acc[r] = fmaf(lds[r * D + k0 + i], w[i], acc[r]);
;         }
	global_load_dword v124, v[4:5], off
	v_add_co_u32_e32 v4, vcc, 0xfff88000, v26
	s_nop 1
	v_addc_co_u32_e32 v5, vcc, -1, v27, vcc
	global_load_dword v126, v[4:5], off
	v_add_co_u32_e32 v4, vcc, 0xfff8e000, v26
	s_nop 1
	v_addc_co_u32_e32 v5, vcc, -1, v27, vcc
	global_load_dword v128, v[4:5], off
	v_add_co_u32_e32 v4, vcc, 0xfff94000, v26
	s_nop 1
	v_addc_co_u32_e32 v5, vcc, -1, v27, vcc
	global_load_dword v130, v[4:5], off
	v_add_co_u32_e32 v4, vcc, 0xfff9a000, v26
	s_nop 1
	v_addc_co_u32_e32 v5, vcc, -1, v27, vcc
	global_load_dword v132, v[4:5], off
	v_add_co_u32_e32 v4, vcc, 0xfffa0000, v26
	s_nop 1
	v_addc_co_u32_e32 v5, vcc, -1, v27, vcc
	global_load_dword v134, v[4:5], off
	v_add_co_u32_e32 v4, vcc, 0xfffa6000, v26
	s_nop 1
	v_addc_co_u32_e32 v5, vcc, -1, v27, vcc
	global_load_dword v136, v[4:5], off
	v_add_co_u32_e32 v4, vcc, 0xfffac000, v26
	s_nop 1
	v_addc_co_u32_e32 v5, vcc, -1, v27, vcc
	global_load_dword v138, v[4:5], off
	v_add_co_u32_e32 v4, vcc, 0xfffb2000, v26
	s_nop 1
	v_addc_co_u32_e32 v5, vcc, -1, v27, vcc
	global_load_dword v140, v[4:5], off
	v_add_co_u32_e32 v4, vcc, 0xfffb8000, v26
	s_nop 1
	v_addc_co_u32_e32 v5, vcc, -1, v27, vcc
	global_load_dword v142, v[4:5], off
	v_add_co_u32_e32 v4, vcc, 0xfffbe000, v26
	s_nop 1
	v_addc_co_u32_e32 v5, vcc, -1, v27, vcc
	global_load_dword v158, v[4:5], off
	v_add_co_u32_e32 v4, vcc, 0xfffc4000, v26
	s_nop 1
	v_addc_co_u32_e32 v5, vcc, -1, v27, vcc
	global_load_dword v160, v[4:5], off
	v_add_co_u32_e32 v4, vcc, 0xfffca000, v26
	s_nop 1
	v_addc_co_u32_e32 v5, vcc, -1, v27, vcc
	global_load_dword v162, v[4:5], off
	v_add_co_u32_e32 v4, vcc, 0xfffd0000, v26
	s_nop 1
	v_addc_co_u32_e32 v5, vcc, -1, v27, vcc
	global_load_dword v164, v[4:5], off
	v_add_co_u32_e32 v4, vcc, 0xfffd6000, v26
	s_nop 1
	v_addc_co_u32_e32 v5, vcc, -1, v27, vcc
	global_load_dword v166, v[4:5], off
	v_add_co_u32_e32 v4, vcc, s7, v26
	s_nop 1
	v_addc_co_u32_e32 v5, vcc, -1, v27, vcc
	global_load_dword v168, v[4:5], off
	v_add_co_u32_e32 v4, vcc, 0xfffe2000, v26
	s_nop 1
	v_addc_co_u32_e32 v5, vcc, -1, v27, vcc
	global_load_dword v170, v[4:5], off
	v_add_co_u32_e32 v4, vcc, 0xfffe8000, v26
	s_nop 1
	v_addc_co_u32_e32 v5, vcc, -1, v27, vcc
	global_load_dword v172, v[4:5], off
	v_add_co_u32_e32 v4, vcc, 0xfffee000, v26
	s_nop 1
	v_addc_co_u32_e32 v5, vcc, -1, v27, vcc
	global_load_dword v174, v[4:5], off
	v_add_co_u32_e32 v4, vcc, 0xffff4000, v26
	s_nop 1
	v_addc_co_u32_e32 v5, vcc, -1, v27, vcc
	global_load_dword v176, v[4:5], off
	v_add_co_u32_e32 v4, vcc, 0xffffa000, v26
	s_nop 1
	v_addc_co_u32_e32 v5, vcc, -1, v27, vcc
	global_load_dword v178, v[4:5], off
	global_load_dword v180, v[26:27], off
	v_lshl_add_u64 v[26:27], v[26:27], 0, s[16:17]
	v_add_u32_e32 v47, 0x304c, v43
	ds_read_b128 v[4:7], v43 offset:16384
	ds_read_b128 v[12:15], v43 offset:16416
	s_waitcnt vmcnt(63) lgkmcnt(1)
	v_fmac_f32_e32 v41, v4, v82
	s_waitcnt vmcnt(62)
	v_fmac_f32_e32 v41, v5, v84
	s_waitcnt vmcnt(61)
	v_fmac_f32_e32 v41, v6, v86
	s_waitcnt vmcnt(60)
	v_fmac_f32_e32 v41, v7, v88
	ds_read_b128 v[4:7], v43 offset:16400
	s_waitcnt vmcnt(59) lgkmcnt(0)
	v_fmac_f32_e32 v41, v4, v74
	s_waitcnt vmcnt(58)
	v_fmac_f32_e32 v41, v5, v76
	s_waitcnt vmcnt(57)
	v_fmac_f32_e32 v41, v6, v78
	s_waitcnt vmcnt(56)
	v_fmac_f32_e32 v41, v7, v80
	ds_read_b128 v[90:93], v43
	ds_read_b128 v[94:97], v43 offset:16
	ds_read_b128 v[8:11], v43 offset:32
	ds_read_b128 v[4:7], v43 offset:48
	ds_read_b128 v[98:101], v43 offset:4096
	s_waitcnt lgkmcnt(4)
	v_mov_b32_e32 v102, v90
	v_mov_b32_e32 v90, v92
	s_waitcnt vmcnt(55)
	v_fmac_f32_e32 v41, v12, v70
	s_waitcnt vmcnt(54)
	v_fmac_f32_e32 v41, v13, v72
	s_waitcnt lgkmcnt(0)
	v_mov_b32_e32 v103, v98
	v_pk_fma_f32 v[16:17], v[102:103], v[82:83], v[16:17] op_sel_hi:[1,0,1]
	v_mov_b32_e32 v98, v91
	v_pk_fma_f32 v[16:17], v[98:99], v[84:85], v[16:17] op_sel_hi:[1,0,1]
	v_mov_b32_e32 v91, v100
	v_pk_fma_f32 v[16:17], v[90:91], v[86:87], v[16:17] op_sel_hi:[1,0,1]
	v_mov_b32_e32 v100, v93
	ds_read_b128 v[90:93], v43 offset:4112
	v_pk_fma_f32 v[16:17], v[100:101], v[88:89], v[16:17] op_sel_hi:[1,0,1]
	v_mov_b32_e32 v98, v94
	v_mov_b32_e32 v94, v8
	s_waitcnt vmcnt(53)
	v_fmac_f32_e32 v41, v14, v66
	s_waitcnt lgkmcnt(0)
	v_mov_b32_e32 v99, v90
	v_pk_fma_f32 v[16:17], v[98:99], v[74:75], v[16:17] op_sel_hi:[1,0,1]
	v_mov_b32_e32 v90, v95
	v_pk_fma_f32 v[16:17], v[90:91], v[76:77], v[16:17] op_sel_hi:[1,0,1]
	v_mov_b32_e32 v90, v96
	v_mov_b32_e32 v91, v92
	v_pk_fma_f32 v[16:17], v[90:91], v[78:79], v[16:17] op_sel_hi:[1,0,1]
	v_mov_b32_e32 v92, v97
	v_pk_fma_f32 v[16:17], v[92:93], v[80:81], v[16:17] op_sel_hi:[1,0,1]
	ds_read_b128 v[90:93], v43 offset:4128
	s_waitcnt vmcnt(52)
	v_fmac_f32_e32 v41, v15, v68
	s_waitcnt lgkmcnt(0)
	v_mov_b32_e32 v95, v90
	v_pk_fma_f32 v[16:17], v[94:95], v[70:71], v[16:17] op_sel_hi:[1,0,1]
	ds_read_b128 v[94:97], v43 offset:8192
	ds_read_b128 v[98:101], v43 offset:12288
	v_mov_b32_e32 v90, v9
	v_pk_fma_f32 v[8:9], v[90:91], v[72:73], v[16:17] op_sel_hi:[1,0,1]
	s_waitcnt lgkmcnt(1)
	v_mov_b32_e32 v16, v94
	s_waitcnt lgkmcnt(0)
	v_mov_b32_e32 v17, v98
	v_pk_fma_f32 v[16:17], v[16:17], v[82:83], v[18:19] op_sel_hi:[1,0,1]
	v_mov_b32_e32 v98, v95
	v_pk_fma_f32 v[16:17], v[98:99], v[84:85], v[16:17] op_sel_hi:[1,0,1]
	v_mov_b32_e32 v18, v96
	v_mov_b32_e32 v19, v100
	v_pk_fma_f32 v[16:17], v[18:19], v[86:87], v[16:17] op_sel_hi:[1,0,1]
	v_mov_b32_e32 v100, v97
	v_pk_fma_f32 v[86:87], v[100:101], v[88:89], v[16:17] op_sel_hi:[1,0,1]
	ds_read_b128 v[16:19], v43 offset:8208
	ds_read_b128 v[82:85], v43 offset:12304
	s_waitcnt lgkmcnt(1)
	v_mov_b32_e32 v88, v16
	s_waitcnt lgkmcnt(0)
;     template <class T> __device__ __forceinline__ T* w(size_t off) const { return (T*)(p->ws + off); }
; __device__ __forceinline__ void ph_prep(Ctx& c, int gtid, int gthreads, int bid, int G, float* lds) {
;     ...
;             for (int i = 0; i < 32; ++i)
; #pragma unroll
;                 for (int r = 0; r < 5; ++r) acc[r] = fmaf(lds[r * D + k0 + i], w[i], acc[r]);
	v_mov_b32_e32 v89, v82
	v_pk_fma_f32 v[74:75], v[88:89], v[74:75], v[86:87] op_sel_hi:[1,0,1]
	v_mov_b32_e32 v82, v17
	v_pk_fma_f32 v[16:17], v[82:83], v[76:77], v[74:75] op_sel_hi:[1,0,1]
	v_mov_b32_e32 v74, v18
	v_mov_b32_e32 v75, v84
	v_pk_fma_f32 v[16:17], v[74:75], v[78:79], v[16:17] op_sel_hi:[1,0,1]
	v_mov_b32_e32 v84, v19
	v_pk_fma_f32 v[16:17], v[84:85], v[80:81], v[16:17] op_sel_hi:[1,0,1]
	ds_read_b128 v[74:77], v43 offset:8224
	ds_read_b128 v[78:81], v43 offset:12320
	ds_read_b128 v[12:15], v43 offset:16432
	v_mov_b32_e32 v82, v4
	s_waitcnt lgkmcnt(2)
	v_mov_b32_e32 v18, v74
	s_waitcnt lgkmcnt(1)
	v_mov_b32_e32 v19, v78
	v_pk_fma_f32 v[16:17], v[18:19], v[70:71], v[16:17] op_sel_hi:[1,0,1]
	v_mov_b32_e32 v78, v75
	s_waitcnt vmcnt(51) lgkmcnt(0)
	v_fmac_f32_e32 v41, v12, v56
	v_pk_fma_f32 v[74:75], v[78:79], v[72:73], v[16:17] op_sel_hi:[1,0,1]
	s_waitcnt vmcnt(50)
	v_fmac_f32_e32 v41, v13, v58
	v_mov_b32_e32 v78, v10
	v_mov_b32_e32 v79, v92
	s_waitcnt vmcnt(49)
	v_fmac_f32_e32 v41, v14, v60
	v_pk_fma_f32 v[8:9], v[78:79], v[66:67], v[8:9] op_sel_hi:[1,0,1]
	v_mov_b32_e32 v92, v11
	s_waitcnt vmcnt(48)
	v_fmac_f32_e32 v41, v15, v62
	ds_read_b128 v[12:15], v43 offset:16448
	ds_read_b96 v[70:72], v43 offset:4160
	ds_read_b96 v[16:18], v43 offset:12352
	v_pk_fma_f32 v[78:79], v[92:93], v[68:69], v[8:9] op_sel_hi:[1,0,1]
	ds_read_b128 v[8:11], v43 offset:4144
	v_add_u32_e32 v19, 0x104c, v43
	s_waitcnt vmcnt(47) lgkmcnt(3)
	v_fmac_f32_e32 v41, v12, v48
	s_waitcnt vmcnt(46)
	v_fmac_f32_e32 v41, v13, v50
	s_waitcnt vmcnt(45)
	v_fmac_f32_e32 v41, v14, v52
	s_waitcnt lgkmcnt(0)
	v_mov_b32_e32 v83, v8
	v_pk_fma_f32 v[78:79], v[82:83], v[56:57], v[78:79] op_sel_hi:[1,0,1]
	v_mov_b32_e32 v8, v5
	v_pk_fma_f32 v[4:5], v[8:9], v[58:59], v[78:79] op_sel_hi:[1,0,1]
	v_mov_b32_e32 v8, v6
	v_mov_b32_e32 v9, v10
	v_pk_fma_f32 v[4:5], v[8:9], v[60:61], v[4:5] op_sel_hi:[1,0,1]
	v_mov_b32_e32 v10, v7
	v_pk_fma_f32 v[8:9], v[10:11], v[62:63], v[4:5] op_sel_hi:[1,0,1]
	ds_read_b128 v[4:7], v43 offset:64
	v_mov_b32_e32 v11, v70
	ds_read_b96 v[12:14], v43 offset:80
	s_waitcnt vmcnt(44)
	v_fmac_f32_e32 v41, v15, v54
	s_waitcnt lgkmcnt(1)
	v_mov_b32_e32 v10, v4
	v_pk_fma_f32 v[8:9], v[10:11], v[48:49], v[8:9] op_sel_hi:[1,0,1]
	v_mov_b32_e32 v70, v5
	v_pk_fma_f32 v[4:5], v[70:71], v[50:51], v[8:9] op_sel_hi:[1,0,1]
	v_mov_b32_e32 v8, v6
	v_mov_b32_e32 v9, v72
	v_pk_fma_f32 v[4:5], v[8:9], v[52:53], v[4:5] op_sel_hi:[1,0,1]
	ds_read2_b32 v[8:9], v19 offset1:1
	s_waitcnt lgkmcnt(0)
	v_pk_mov_b32 v[6:7], v[6:7], v[8:9] op_sel:[1,0]
	s_nop 0
	v_pk_fma_f32 v[4:5], v[6:7], v[54:55], v[4:5] op_sel_hi:[1,0,1]
	v_mov_b32_e32 v8, v12
	s_waitcnt vmcnt(43)
	v_pk_fma_f32 v[70:71], v[8:9], v[46:47], v[4:5] op_sel_hi:[1,0,1]
	v_mov_b32_e32 v4, v76
	v_mov_b32_e32 v5, v80
	v_pk_fma_f32 v[4:5], v[4:5], v[66:67], v[74:75] op_sel_hi:[1,0,1]
	v_mov_b32_e32 v80, v77
	ds_read_b96 v[8:10], v43 offset:8272
	v_pk_fma_f32 v[72:73], v[80:81], v[68:69], v[4:5] op_sel_hi:[1,0,1]
	ds_read_b128 v[4:7], v43 offset:8240
	ds_read_b128 v[66:69], v43 offset:12336
	ds_read_b32 v11, v43 offset:12404
	ds_read_b32 v15, v43 offset:4212
	v_mov_b32_e32 v12, v13
	s_waitcnt lgkmcnt(3)
	v_mov_b32_e32 v74, v4
	s_waitcnt lgkmcnt(2)
	v_mov_b32_e32 v75, v66
	v_pk_fma_f32 v[56:57], v[74:75], v[56:57], v[72:73] op_sel_hi:[1,0,1]
	v_mov_b32_e32 v66, v5
	v_pk_fma_f32 v[4:5], v[66:67], v[58:59], v[56:57] op_sel_hi:[1,0,1]
	v_mov_b32_e32 v56, v6
	v_mov_b32_e32 v57, v68
	v_pk_fma_f32 v[4:5], v[56:57], v[60:61], v[4:5] op_sel_hi:[1,0,1]
	v_mov_b32_e32 v68, v7
	v_pk_fma_f32 v[56:57], v[68:69], v[62:63], v[4:5] op_sel_hi:[1,0,1]
	ds_read_b128 v[4:7], v43 offset:8256
	v_mov_b32_e32 v59, v16
	s_waitcnt lgkmcnt(0)
	v_mov_b32_e32 v58, v4
	v_pk_fma_f32 v[48:49], v[58:59], v[48:49], v[56:57] op_sel_hi:[1,0,1]
	v_mov_b32_e32 v16, v5
	v_pk_fma_f32 v[4:5], v[16:17], v[50:51], v[48:49] op_sel_hi:[1,0,1]
	v_mov_b32_e32 v16, v6
	v_mov_b32_e32 v17, v18
	v_pk_fma_f32 v[4:5], v[16:17], v[52:53], v[4:5] op_sel_hi:[1,0,1]
	ds_read2_b32 v[16:17], v47 offset1:1
	v_add_u32_e32 v53, 0x1064, v43
	v_add_u32_e32 v56, 0x106c, v43
	v_add_u32_e32 v50, 0x3054, v43
	v_add_u32_e32 v51, 0x205c, v43
	s_waitcnt lgkmcnt(0)
	v_pk_mov_b32 v[6:7], v[6:7], v[16:17] op_sel:[1,0]
	v_mov_b32_e32 v16, v8
	v_pk_fma_f32 v[4:5], v[6:7], v[54:55], v[4:5] op_sel_hi:[1,0,1]
	v_add_u32_e32 v8, 0x1054, v43
	v_pk_fma_f32 v[18:19], v[16:17], v[46:47], v[4:5] op_sel_hi:[1,0,1]
	ds_read_b128 v[4:7], v43 offset:16464
	v_add_u32_e32 v52, 0x305c, v43
	v_add_u32_e32 v54, 0x2064, v43
	v_add_u32_e32 v55, 0x3064, v43
	v_add_u32_e32 v57, 0x206c, v43
	s_waitcnt lgkmcnt(0)
	v_fmac_f32_e32 v41, v4, v46
	s_waitcnt vmcnt(42)
	v_fmac_f32_e32 v41, v5, v2
	s_waitcnt vmcnt(41)
	v_fmac_f32_e32 v41, v6, v30
	s_waitcnt vmcnt(40)
	v_fmac_f32_e32 v41, v7, v28
	ds_read_b128 v[4:7], v43 offset:16480
	v_add_u32_e32 v46, 0x105c, v43
	v_add_u32_e32 v58, 0x306c, v43
	v_add_u32_e32 v59, 0x2074, v43
	s_waitcnt vmcnt(39) lgkmcnt(0)
	v_fmac_f32_e32 v41, v4, v32
	s_waitcnt vmcnt(38)
	v_fmac_f32_e32 v41, v5, v36
	s_waitcnt vmcnt(37)
	v_fmac_f32_e32 v41, v6, v40
	s_waitcnt vmcnt(36)
	v_fmac_f32_e32 v41, v7, v38
	ds_read_b128 v[4:7], v43 offset:16496
	s_waitcnt vmcnt(35) lgkmcnt(0)
	v_fmac_f32_e32 v41, v4, v42
	ds_read_b32 v4, v43 offset:124
	ds_read2_b32 v[16:17], v8 offset1:1
	s_waitcnt vmcnt(34)
	v_fmac_f32_e32 v41, v5, v44
	s_waitcnt vmcnt(33)
	v_fmac_f32_e32 v41, v6, v34
	v_mov_b32_e32 v8, v9
	s_waitcnt lgkmcnt(0)
	v_mov_b32_e32 v13, v16
	v_pk_fma_f32 v[12:13], v[12:13], v[2:3], v[70:71] op_sel_hi:[1,0,1]
	v_mov_b32_e32 v16, v14
	v_pk_fma_f32 v[12:13], v[16:17], v[30:31], v[12:13] op_sel_hi:[1,0,1]
	ds_read2_b32 v[16:17], v43 offset0:23 offset1:24
	ds_read2_b32 v[46:47], v46 offset1:1
	s_waitcnt lgkmcnt(1)
;     template <class T> __device__ __forceinline__ T* w(size_t off) const { return (T*)(p->ws + off); }
; __device__ __forceinline__ void ph_prep(Ctx& c, int gtid, int gthreads, int bid, int G, float* lds) {
;     ...
;         for (int k0 = kq * 256; k0 < kq * 256 + 256; k0 += 32) {
;             float w[32];
; #pragma unroll
;             for (int i = 0; i < 32; ++i) w[i] = aw[(size_t)(k0 + i) * 6144];
; #pragma unroll
;             for (int i = 0; i < 32; ++i)
; #pragma unroll
;                 for (int r = 0; r < 5; ++r) acc[r] = fmaf(lds[r * D + k0 + i], w[i], acc[r]);
;         }
	v_mov_b32_e32 v48, v16
	s_waitcnt lgkmcnt(0)
	v_mov_b32_e32 v49, v46
	v_pk_fma_f32 v[12:13], v[48:49], v[28:29], v[12:13] op_sel_hi:[1,0,1]
	v_mov_b32_e32 v46, v17
	v_pk_fma_f32 v[12:13], v[46:47], v[32:33], v[12:13] op_sel_hi:[1,0,1]
	ds_read2_b32 v[16:17], v43 offset0:25 offset1:26
	ds_read2_b32 v[46:47], v53 offset1:1
	s_waitcnt lgkmcnt(1)
	v_mov_b32_e32 v48, v16
	s_waitcnt lgkmcnt(0)
	v_mov_b32_e32 v49, v46
	v_pk_fma_f32 v[12:13], v[48:49], v[36:37], v[12:13] op_sel_hi:[1,0,1]
	v_mov_b32_e32 v46, v17
	v_pk_fma_f32 v[12:13], v[46:47], v[40:41], v[12:13] op_sel_hi:[1,0,1]
	ds_read2_b32 v[16:17], v43 offset0:27 offset1:28
	ds_read2_b32 v[46:47], v56 offset1:1
	s_waitcnt lgkmcnt(1)
	v_mov_b32_e32 v48, v16
	s_waitcnt lgkmcnt(0)
	v_mov_b32_e32 v49, v46
	v_mov_b32_e32 v46, v17
	ds_read2_b32 v[16:17], v43 offset0:29 offset1:30
	v_pk_fma_f32 v[12:13], v[48:49], v[38:39], v[12:13] op_sel_hi:[1,0,1]
	s_waitcnt lgkmcnt(0)
	v_mov_b32_e32 v14, v16
	v_pk_fma_f32 v[12:13], v[46:47], v[42:43], v[12:13] op_sel_hi:[1,0,1]
	s_nop 0
	v_pk_fma_f32 v[12:13], v[14:15], v[44:45], v[12:13] op_sel_hi:[1,0,1]
	ds_read_b64 v[14:15], v43 offset:4216
	s_waitcnt lgkmcnt(0)
	v_pk_mov_b32 v[16:17], v[16:17], v[14:15] op_sel:[1,0]
	s_nop 0
	v_pk_fma_f32 v[12:13], v[16:17], v[34:35], v[12:13] op_sel_hi:[1,0,1]
	v_mov_b32_e32 v5, v15
	s_waitcnt vmcnt(32)
	v_pk_fma_f32 v[16:17], v[4:5], v[64:65], v[12:13] op_sel_hi:[1,0,1]
	ds_read_b32 v4, v43 offset:8316
	ds_read2_b32 v[12:13], v50 offset1:1
	s_waitcnt lgkmcnt(0)
	v_mov_b32_e32 v9, v12
	v_pk_fma_f32 v[8:9], v[8:9], v[2:3], v[18:19] op_sel_hi:[1,0,1]
	v_mov_b32_e32 v12, v10
	v_pk_fma_f32 v[8:9], v[12:13], v[30:31], v[8:9] op_sel_hi:[1,0,1]
	ds_read2_b32 v[12:13], v51 offset1:1
	ds_read2_b32 v[14:15], v52 offset1:1
	s_waitcnt lgkmcnt(1)
	v_mov_b32_e32 v18, v12
	s_waitcnt lgkmcnt(0)
	v_mov_b32_e32 v19, v14
	v_pk_fma_f32 v[8:9], v[18:19], v[28:29], v[8:9] op_sel_hi:[1,0,1]
	v_mov_b32_e32 v14, v13
	v_pk_fma_f32 v[8:9], v[14:15], v[32:33], v[8:9] op_sel_hi:[1,0,1]
	ds_read2_b32 v[12:13], v54 offset1:1
	ds_read2_b32 v[14:15], v55 offset1:1
	s_waitcnt lgkmcnt(1)
	v_mov_b32_e32 v18, v12
	s_waitcnt lgkmcnt(0)
	v_mov_b32_e32 v19, v14
	v_pk_fma_f32 v[8:9], v[18:19], v[36:37], v[8:9] op_sel_hi:[1,0,1]
	v_mov_b32_e32 v14, v13
	v_pk_fma_f32 v[8:9], v[14:15], v[40:41], v[8:9] op_sel_hi:[1,0,1]
	ds_read2_b32 v[12:13], v57 offset1:1
	ds_read2_b32 v[14:15], v58 offset1:1
	v_fmac_f32_e32 v41, v7, v64
	s_waitcnt lgkmcnt(1)
	v_mov_b32_e32 v18, v12
	s_waitcnt lgkmcnt(0)
	v_mov_b32_e32 v19, v14
	v_mov_b32_e32 v14, v13
	ds_read2_b32 v[12:13], v59 offset1:1
	v_pk_fma_f32 v[8:9], v[18:19], v[38:39], v[8:9] op_sel_hi:[1,0,1]
	s_waitcnt lgkmcnt(0)
	v_mov_b32_e32 v10, v12
	v_pk_fma_f32 v[8:9], v[14:15], v[42:43], v[8:9] op_sel_hi:[1,0,1]
	s_nop 0
	v_pk_fma_f32 v[8:9], v[10:11], v[44:45], v[8:9] op_sel_hi:[1,0,1]
	ds_read_b64 v[10:11], v43 offset:12408
	v_add_u32_e32 v45, 32, v45
	v_add_u32_e32 v43, 0x80, v43
	s_waitcnt lgkmcnt(0)
	v_pk_mov_b32 v[12:13], v[12:13], v[10:11] op_sel:[1,0]
	v_mov_b32_e32 v5, v11
	v_pk_fma_f32 v[8:9], v[12:13], v[34:35], v[8:9] op_sel_hi:[1,0,1]
	s_nop 0
	v_pk_fma_f32 v[18:19], v[4:5], v[64:65], v[8:9] op_sel_hi:[1,0,1]
	s_cmp_eq_u32 s98, 3
	s_cbranch_scc1 .Lmod_last
	v_add_co_u32_e32 v4, vcc, 0xfff46000, v26
	s_mov_b32 s7, 0xfffdc000
	s_nop 0
	v_addc_co_u32_e32 v5, vcc, -1, v27, vcc
	global_load_dword v82, v[4:5], off
	v_add_co_u32_e32 v4, vcc, 0xfff4c000, v26
	s_nop 0
	s_nop 0
	v_addc_co_u32_e32 v5, vcc, -1, v27, vcc
	global_load_dword v84, v[4:5], off
	v_add_co_u32_e32 v4, vcc, 0xfff52000, v26
	s_nop 0
	s_nop 0
	v_addc_co_u32_e32 v5, vcc, -1, v27, vcc
	global_load_dword v86, v[4:5], off
	v_add_co_u32_e32 v4, vcc, 0xfff58000, v26
	s_nop 1
	v_addc_co_u32_e32 v5, vcc, -1, v27, vcc
	global_load_dword v88, v[4:5], off
	v_add_co_u32_e32 v4, vcc, 0xfff5e000, v26
	s_nop 1
	v_addc_co_u32_e32 v5, vcc, -1, v27, vcc
	global_load_dword v74, v[4:5], off
	v_add_co_u32_e32 v4, vcc, 0xfff64000, v26
	s_nop 1
	v_addc_co_u32_e32 v5, vcc, -1, v27, vcc
	global_load_dword v76, v[4:5], off
	v_add_co_u32_e32 v4, vcc, 0xfff6a000, v26
	s_nop 1
	v_addc_co_u32_e32 v5, vcc, -1, v27, vcc
	global_load_dword v78, v[4:5], off
	v_add_co_u32_e32 v4, vcc, 0xfff70000, v26
	s_nop 1
	v_addc_co_u32_e32 v5, vcc, -1, v27, vcc
	global_load_dword v80, v[4:5], off
	v_add_co_u32_e32 v4, vcc, 0xfff76000, v26
	s_nop 1
	v_addc_co_u32_e32 v5, vcc, -1, v27, vcc
	global_load_dword v70, v[4:5], off
	v_add_co_u32_e32 v4, vcc, 0xfff7c000, v26
	s_nop 1
	v_addc_co_u32_e32 v5, vcc, -1, v27, vcc
	global_load_dword v72, v[4:5], off
	v_add_co_u32_e32 v4, vcc, 0xfff82000, v26
	s_nop 1
	v_addc_co_u32_e32 v5, vcc, -1, v27, vcc
	global_load_dword v66, v[4:5], off
	v_add_co_u32_e32 v4, vcc, 0xfff88000, v26
	s_nop 1
	v_addc_co_u32_e32 v5, vcc, -1, v27, vcc
	global_load_dword v68, v[4:5], off
	v_add_co_u32_e32 v4, vcc, 0xfff8e000, v26
	s_nop 1
	v_addc_co_u32_e32 v5, vcc, -1, v27, vcc
	global_load_dword v56, v[4:5], off
	v_add_co_u32_e32 v4, vcc, 0xfff94000, v26
	s_nop 1
	v_addc_co_u32_e32 v5, vcc, -1, v27, vcc
	global_load_dword v58, v[4:5], off
	v_add_co_u32_e32 v4, vcc, 0xfff9a000, v26
	s_nop 1
	v_addc_co_u32_e32 v5, vcc, -1, v27, vcc
	global_load_dword v60, v[4:5], off
	v_add_co_u32_e32 v4, vcc, 0xfffa0000, v26
	s_nop 1
	v_addc_co_u32_e32 v5, vcc, -1, v27, vcc
	global_load_dword v62, v[4:5], off
	v_add_co_u32_e32 v4, vcc, 0xfffa6000, v26
	s_nop 1
	v_addc_co_u32_e32 v5, vcc, -1, v27, vcc
	global_load_dword v48, v[4:5], off
	v_add_co_u32_e32 v4, vcc, 0xfffac000, v26
	s_nop 1
	v_addc_co_u32_e32 v5, vcc, -1, v27, vcc
	global_load_dword v50, v[4:5], off
	v_add_co_u32_e32 v4, vcc, 0xfffb2000, v26
;     template <class T> __device__ __forceinline__ T* w(size_t off) const { return (T*)(p->ws + off); }
; __device__ __forceinline__ void ph_prep(Ctx& c, int gtid, int gthreads, int bid, int G, float* lds) {
;     ...
;         for (int k0 = kq * 256; k0 < kq * 256 + 256; k0 += 32) {
;             float w[32];
; #pragma unroll
;             for (int i = 0; i < 32; ++i) w[i] = aw[(size_t)(k0 + i) * 6144];
; #pragma unroll
;             for (int i = 0; i < 32; ++i)
; #pragma unroll
;                 for (int r = 0; r < 5; ++r) acc[r] = fmaf(lds[r * D + k0 + i], w[i], acc[r]);
;         }
	s_nop 1
	v_addc_co_u32_e32 v5, vcc, -1, v27, vcc
	global_load_dword v52, v[4:5], off
	v_add_co_u32_e32 v4, vcc, 0xfffb8000, v26
	s_nop 1
	v_addc_co_u32_e32 v5, vcc, -1, v27, vcc
	global_load_dword v54, v[4:5], off
	v_add_co_u32_e32 v4, vcc, 0xfffbe000, v26
	s_nop 1
	v_addc_co_u32_e32 v5, vcc, -1, v27, vcc
	global_load_dword v46, v[4:5], off
	v_add_co_u32_e32 v4, vcc, 0xfffc4000, v26
	s_nop 1
	v_addc_co_u32_e32 v5, vcc, -1, v27, vcc
	global_load_dword v2, v[4:5], off
	v_add_co_u32_e32 v4, vcc, 0xfffca000, v26
	s_nop 1
	v_addc_co_u32_e32 v5, vcc, -1, v27, vcc
	global_load_dword v30, v[4:5], off
	v_add_co_u32_e32 v4, vcc, 0xfffd0000, v26
	s_nop 1
	v_addc_co_u32_e32 v5, vcc, -1, v27, vcc
	global_load_dword v28, v[4:5], off
	v_add_co_u32_e32 v4, vcc, 0xfffd6000, v26
	s_nop 1
	v_addc_co_u32_e32 v5, vcc, -1, v27, vcc
	global_load_dword v32, v[4:5], off
	v_add_co_u32_e32 v4, vcc, s7, v26
	s_nop 1
	v_addc_co_u32_e32 v5, vcc, -1, v27, vcc
	global_load_dword v36, v[4:5], off
	v_add_co_u32_e32 v4, vcc, 0xfffe2000, v26
	s_nop 1
	v_addc_co_u32_e32 v5, vcc, -1, v27, vcc
	global_load_dword v40, v[4:5], off
	v_add_co_u32_e32 v4, vcc, 0xfffe8000, v26
	s_nop 1
	v_addc_co_u32_e32 v5, vcc, -1, v27, vcc
	global_load_dword v38, v[4:5], off
	v_add_co_u32_e32 v4, vcc, 0xfffee000, v26
	s_nop 1
	v_addc_co_u32_e32 v5, vcc, -1, v27, vcc
	global_load_dword v42, v[4:5], off
	v_add_co_u32_e32 v4, vcc, 0xffff4000, v26
	s_nop 1
	v_addc_co_u32_e32 v5, vcc, -1, v27, vcc
	global_load_dword v44, v[4:5], off
	v_add_co_u32_e32 v4, vcc, 0xffffa000, v26
	s_nop 1
	v_addc_co_u32_e32 v5, vcc, -1, v27, vcc
	global_load_dword v34, v[4:5], off
	global_load_dword v64, v[26:27], off
	v_lshl_add_u64 v[26:27], v[26:27], 0, s[16:17]
	v_add_u32_e32 v159, 0x304c, v43
	ds_read_b128 v[4:7], v43 offset:16384
	ds_read_b128 v[12:15], v43 offset:16416
	s_waitcnt vmcnt(63) lgkmcnt(1)
	v_fmac_f32_e32 v41, v4, v104
	s_waitcnt vmcnt(62)
	v_fmac_f32_e32 v41, v5, v106
	s_waitcnt vmcnt(61)
	v_fmac_f32_e32 v41, v6, v108
	s_waitcnt vmcnt(60)
	v_fmac_f32_e32 v41, v7, v110
	ds_read_b128 v[4:7], v43 offset:16400
	s_waitcnt vmcnt(59) lgkmcnt(0)
	v_fmac_f32_e32 v41, v4, v112
	s_waitcnt vmcnt(58)
	v_fmac_f32_e32 v41, v5, v114
	s_waitcnt vmcnt(57)
	v_fmac_f32_e32 v41, v6, v116
	s_waitcnt vmcnt(56)
	v_fmac_f32_e32 v41, v7, v118
	ds_read_b128 v[90:93], v43
	ds_read_b128 v[94:97], v43 offset:16
	ds_read_b128 v[8:11], v43 offset:32
	ds_read_b128 v[4:7], v43 offset:48
	ds_read_b128 v[98:101], v43 offset:4096
	s_waitcnt lgkmcnt(4)
	v_mov_b32_e32 v102, v90
	v_mov_b32_e32 v90, v92
	s_waitcnt vmcnt(55)
	v_fmac_f32_e32 v41, v12, v120
	s_waitcnt vmcnt(54)
	v_fmac_f32_e32 v41, v13, v122
	s_waitcnt lgkmcnt(0)
	v_mov_b32_e32 v103, v98
	v_pk_fma_f32 v[16:17], v[102:103], v[104:105], v[16:17] op_sel_hi:[1,0,1]
	v_mov_b32_e32 v98, v91
	v_pk_fma_f32 v[16:17], v[98:99], v[106:107], v[16:17] op_sel_hi:[1,0,1]
	v_mov_b32_e32 v91, v100
	v_pk_fma_f32 v[16:17], v[90:91], v[108:109], v[16:17] op_sel_hi:[1,0,1]
	v_mov_b32_e32 v100, v93
	ds_read_b128 v[90:93], v43 offset:4112
	v_pk_fma_f32 v[16:17], v[100:101], v[110:111], v[16:17] op_sel_hi:[1,0,1]
	v_mov_b32_e32 v98, v94
	v_mov_b32_e32 v94, v8
	s_waitcnt vmcnt(53)
	v_fmac_f32_e32 v41, v14, v124
	s_waitcnt lgkmcnt(0)
	v_mov_b32_e32 v99, v90
	v_pk_fma_f32 v[16:17], v[98:99], v[112:113], v[16:17] op_sel_hi:[1,0,1]
	v_mov_b32_e32 v90, v95
	v_pk_fma_f32 v[16:17], v[90:91], v[114:115], v[16:17] op_sel_hi:[1,0,1]
	v_mov_b32_e32 v90, v96
	v_mov_b32_e32 v91, v92
	v_pk_fma_f32 v[16:17], v[90:91], v[116:117], v[16:17] op_sel_hi:[1,0,1]
	v_mov_b32_e32 v92, v97
	v_pk_fma_f32 v[16:17], v[92:93], v[118:119], v[16:17] op_sel_hi:[1,0,1]
	ds_read_b128 v[90:93], v43 offset:4128
	s_waitcnt vmcnt(52)
	v_fmac_f32_e32 v41, v15, v126
	s_waitcnt lgkmcnt(0)
	v_mov_b32_e32 v95, v90
	v_pk_fma_f32 v[16:17], v[94:95], v[120:121], v[16:17] op_sel_hi:[1,0,1]
	ds_read_b128 v[94:97], v43 offset:8192
	ds_read_b128 v[98:101], v43 offset:12288
	v_mov_b32_e32 v90, v9
	v_pk_fma_f32 v[8:9], v[90:91], v[122:123], v[16:17] op_sel_hi:[1,0,1]
	s_waitcnt lgkmcnt(1)
	v_mov_b32_e32 v16, v94
	s_waitcnt lgkmcnt(0)
	v_mov_b32_e32 v17, v98
	v_pk_fma_f32 v[16:17], v[16:17], v[104:105], v[18:19] op_sel_hi:[1,0,1]
	v_mov_b32_e32 v98, v95
	v_pk_fma_f32 v[16:17], v[98:99], v[106:107], v[16:17] op_sel_hi:[1,0,1]
	v_mov_b32_e32 v18, v96
	v_mov_b32_e32 v19, v100
	v_pk_fma_f32 v[16:17], v[18:19], v[108:109], v[16:17] op_sel_hi:[1,0,1]
	v_mov_b32_e32 v100, v97
	v_pk_fma_f32 v[108:109], v[100:101], v[110:111], v[16:17] op_sel_hi:[1,0,1]
	ds_read_b128 v[16:19], v43 offset:8208
	ds_read_b128 v[104:107], v43 offset:12304
	s_waitcnt lgkmcnt(1)
	v_mov_b32_e32 v110, v16
	s_waitcnt lgkmcnt(0)
	v_mov_b32_e32 v111, v104
	v_pk_fma_f32 v[112:113], v[110:111], v[112:113], v[108:109] op_sel_hi:[1,0,1]
	v_mov_b32_e32 v104, v17
	v_pk_fma_f32 v[16:17], v[104:105], v[114:115], v[112:113] op_sel_hi:[1,0,1]
	v_mov_b32_e32 v112, v18
	v_mov_b32_e32 v113, v106
	v_pk_fma_f32 v[16:17], v[112:113], v[116:117], v[16:17] op_sel_hi:[1,0,1]
	v_mov_b32_e32 v106, v19
	v_pk_fma_f32 v[16:17], v[106:107], v[118:119], v[16:17] op_sel_hi:[1,0,1]
	ds_read_b128 v[112:115], v43 offset:8224
	ds_read_b128 v[116:119], v43 offset:12320
	ds_read_b128 v[12:15], v43 offset:16432
	v_mov_b32_e32 v104, v4
	s_waitcnt lgkmcnt(2)
	v_mov_b32_e32 v18, v112
	s_waitcnt lgkmcnt(1)
	v_mov_b32_e32 v19, v116
	v_pk_fma_f32 v[16:17], v[18:19], v[120:121], v[16:17] op_sel_hi:[1,0,1]
	v_mov_b32_e32 v116, v113
	s_waitcnt vmcnt(51) lgkmcnt(0)
	v_fmac_f32_e32 v41, v12, v128
	v_pk_fma_f32 v[112:113], v[116:117], v[122:123], v[16:17] op_sel_hi:[1,0,1]
	s_waitcnt vmcnt(50)
;     template <class T> __device__ __forceinline__ T* w(size_t off) const { return (T*)(p->ws + off); }
; __device__ __forceinline__ void ph_prep(Ctx& c, int gtid, int gthreads, int bid, int G, float* lds) {
;     ...
;             for (int i = 0; i < 32; ++i)
; #pragma unroll
;                 for (int r = 0; r < 5; ++r) acc[r] = fmaf(lds[r * D + k0 + i], w[i], acc[r]);
	v_fmac_f32_e32 v41, v13, v130
	v_mov_b32_e32 v116, v10
	v_mov_b32_e32 v117, v92
	s_waitcnt vmcnt(49)
	v_fmac_f32_e32 v41, v14, v132
	v_pk_fma_f32 v[8:9], v[116:117], v[124:125], v[8:9] op_sel_hi:[1,0,1]
	v_mov_b32_e32 v92, v11
	s_waitcnt vmcnt(48)
	v_fmac_f32_e32 v41, v15, v134
	ds_read_b128 v[12:15], v43 offset:16448
	ds_read_b96 v[120:122], v43 offset:4160
	ds_read_b96 v[16:18], v43 offset:12352
	v_pk_fma_f32 v[116:117], v[92:93], v[126:127], v[8:9] op_sel_hi:[1,0,1]
	ds_read_b128 v[8:11], v43 offset:4144
	v_add_u32_e32 v19, 0x104c, v43
	s_waitcnt vmcnt(47) lgkmcnt(3)
	v_fmac_f32_e32 v41, v12, v136
	s_waitcnt vmcnt(46)
	v_fmac_f32_e32 v41, v13, v138
	s_waitcnt vmcnt(45)
	v_fmac_f32_e32 v41, v14, v140
	s_waitcnt lgkmcnt(0)
	v_mov_b32_e32 v105, v8
	v_pk_fma_f32 v[116:117], v[104:105], v[128:129], v[116:117] op_sel_hi:[1,0,1]
	v_mov_b32_e32 v8, v5
	v_pk_fma_f32 v[4:5], v[8:9], v[130:131], v[116:117] op_sel_hi:[1,0,1]
	v_mov_b32_e32 v8, v6
	v_mov_b32_e32 v9, v10
	v_pk_fma_f32 v[4:5], v[8:9], v[132:133], v[4:5] op_sel_hi:[1,0,1]
	v_mov_b32_e32 v10, v7
	v_pk_fma_f32 v[8:9], v[10:11], v[134:135], v[4:5] op_sel_hi:[1,0,1]
	ds_read_b128 v[4:7], v43 offset:64
	v_mov_b32_e32 v11, v120
	ds_read_b96 v[12:14], v43 offset:80
	s_waitcnt vmcnt(44)
	v_fmac_f32_e32 v41, v15, v142
	s_waitcnt lgkmcnt(1)
	v_mov_b32_e32 v10, v4
	v_pk_fma_f32 v[8:9], v[10:11], v[136:137], v[8:9] op_sel_hi:[1,0,1]
	v_mov_b32_e32 v120, v5
	v_pk_fma_f32 v[4:5], v[120:121], v[138:139], v[8:9] op_sel_hi:[1,0,1]
	v_mov_b32_e32 v8, v6
	v_mov_b32_e32 v9, v122
	v_pk_fma_f32 v[4:5], v[8:9], v[140:141], v[4:5] op_sel_hi:[1,0,1]
	ds_read2_b32 v[8:9], v19 offset1:1
	s_waitcnt lgkmcnt(0)
	v_pk_mov_b32 v[6:7], v[6:7], v[8:9] op_sel:[1,0]
	s_nop 0
	v_pk_fma_f32 v[4:5], v[6:7], v[142:143], v[4:5] op_sel_hi:[1,0,1]
	v_mov_b32_e32 v8, v12
	s_waitcnt vmcnt(43)
	v_pk_fma_f32 v[120:121], v[8:9], v[158:159], v[4:5] op_sel_hi:[1,0,1]
	v_mov_b32_e32 v4, v114
	v_mov_b32_e32 v5, v118
	v_pk_fma_f32 v[4:5], v[4:5], v[124:125], v[112:113] op_sel_hi:[1,0,1]
	v_mov_b32_e32 v118, v115
	ds_read_b96 v[8:10], v43 offset:8272
	v_pk_fma_f32 v[122:123], v[118:119], v[126:127], v[4:5] op_sel_hi:[1,0,1]
	ds_read_b128 v[4:7], v43 offset:8240
	ds_read_b128 v[124:127], v43 offset:12336
	ds_read_b32 v11, v43 offset:12404
	ds_read_b32 v15, v43 offset:4212
	v_mov_b32_e32 v12, v13
	s_waitcnt lgkmcnt(3)
	v_mov_b32_e32 v112, v4
	s_waitcnt lgkmcnt(2)
	v_mov_b32_e32 v113, v124
	v_pk_fma_f32 v[128:129], v[112:113], v[128:129], v[122:123] op_sel_hi:[1,0,1]
	v_mov_b32_e32 v124, v5
	v_pk_fma_f32 v[4:5], v[124:125], v[130:131], v[128:129] op_sel_hi:[1,0,1]
	v_mov_b32_e32 v128, v6
	v_mov_b32_e32 v129, v126
	v_pk_fma_f32 v[4:5], v[128:129], v[132:133], v[4:5] op_sel_hi:[1,0,1]
	v_mov_b32_e32 v126, v7
	v_pk_fma_f32 v[128:129], v[126:127], v[134:135], v[4:5] op_sel_hi:[1,0,1]
	ds_read_b128 v[4:7], v43 offset:8256
	v_mov_b32_e32 v131, v16
	s_waitcnt lgkmcnt(0)
	v_mov_b32_e32 v130, v4
	v_pk_fma_f32 v[136:137], v[130:131], v[136:137], v[128:129] op_sel_hi:[1,0,1]
	v_mov_b32_e32 v16, v5
	v_pk_fma_f32 v[4:5], v[16:17], v[138:139], v[136:137] op_sel_hi:[1,0,1]
	v_mov_b32_e32 v16, v6
	v_mov_b32_e32 v17, v18
	v_pk_fma_f32 v[4:5], v[16:17], v[140:141], v[4:5] op_sel_hi:[1,0,1]
	ds_read2_b32 v[16:17], v159 offset1:1
	v_add_u32_e32 v141, 0x1064, v43
	v_add_u32_e32 v128, 0x106c, v43
	v_add_u32_e32 v138, 0x3054, v43
	v_add_u32_e32 v139, 0x205c, v43
	s_waitcnt lgkmcnt(0)
	v_pk_mov_b32 v[6:7], v[6:7], v[16:17] op_sel:[1,0]
	v_mov_b32_e32 v16, v8
	v_pk_fma_f32 v[4:5], v[6:7], v[142:143], v[4:5] op_sel_hi:[1,0,1]
	v_add_u32_e32 v8, 0x1054, v43
	v_pk_fma_f32 v[18:19], v[16:17], v[158:159], v[4:5] op_sel_hi:[1,0,1]
	ds_read_b128 v[4:7], v43 offset:16464
	v_add_u32_e32 v140, 0x305c, v43
	v_add_u32_e32 v142, 0x2064, v43
	v_add_u32_e32 v143, 0x3064, v43
	v_add_u32_e32 v129, 0x206c, v43
	s_waitcnt lgkmcnt(0)
	v_fmac_f32_e32 v41, v4, v158
	s_waitcnt vmcnt(42)
	v_fmac_f32_e32 v41, v5, v160
	s_waitcnt vmcnt(41)
	v_fmac_f32_e32 v41, v6, v162
	s_waitcnt vmcnt(40)
	v_fmac_f32_e32 v41, v7, v164
	ds_read_b128 v[4:7], v43 offset:16480
	v_add_u32_e32 v158, 0x105c, v43
	v_add_u32_e32 v130, 0x306c, v43
	v_add_u32_e32 v131, 0x2074, v43
	s_waitcnt vmcnt(39) lgkmcnt(0)
	v_fmac_f32_e32 v41, v4, v166
	s_waitcnt vmcnt(38)
	v_fmac_f32_e32 v41, v5, v168
	s_waitcnt vmcnt(37)
	v_fmac_f32_e32 v41, v6, v170
	s_waitcnt vmcnt(36)
	v_fmac_f32_e32 v41, v7, v172
	ds_read_b128 v[4:7], v43 offset:16496
	s_waitcnt vmcnt(35) lgkmcnt(0)
	v_fmac_f32_e32 v41, v4, v174
	ds_read_b32 v4, v43 offset:124
	ds_read2_b32 v[16:17], v8 offset1:1
	s_waitcnt vmcnt(34)
	v_fmac_f32_e32 v41, v5, v176
	s_waitcnt vmcnt(33)
	v_fmac_f32_e32 v41, v6, v178
	v_mov_b32_e32 v8, v9
	s_waitcnt lgkmcnt(0)
	v_mov_b32_e32 v13, v16
	v_pk_fma_f32 v[12:13], v[12:13], v[160:161], v[120:121] op_sel_hi:[1,0,1]
	v_mov_b32_e32 v16, v14
	v_pk_fma_f32 v[12:13], v[16:17], v[162:163], v[12:13] op_sel_hi:[1,0,1]
	ds_read2_b32 v[16:17], v43 offset0:23 offset1:24
	ds_read2_b32 v[158:159], v158 offset1:1
	s_waitcnt lgkmcnt(1)
	v_mov_b32_e32 v136, v16
	s_waitcnt lgkmcnt(0)
	v_mov_b32_e32 v137, v158
	v_pk_fma_f32 v[12:13], v[136:137], v[164:165], v[12:13] op_sel_hi:[1,0,1]
	v_mov_b32_e32 v158, v17
	v_pk_fma_f32 v[12:13], v[158:159], v[166:167], v[12:13] op_sel_hi:[1,0,1]
	ds_read2_b32 v[16:17], v43 offset0:25 offset1:26
	ds_read2_b32 v[158:159], v141 offset1:1
	s_waitcnt lgkmcnt(1)
	v_mov_b32_e32 v136, v16
	s_waitcnt lgkmcnt(0)
	v_mov_b32_e32 v137, v158
	v_pk_fma_f32 v[12:13], v[136:137], v[168:169], v[12:13] op_sel_hi:[1,0,1]
	v_mov_b32_e32 v158, v17
	v_pk_fma_f32 v[12:13], v[158:159], v[170:171], v[12:13] op_sel_hi:[1,0,1]
	ds_read2_b32 v[16:17], v43 offset0:27 offset1:28
	ds_read2_b32 v[158:159], v128 offset1:1
	s_waitcnt lgkmcnt(1)
;     template <class T> __device__ __forceinline__ T* w(size_t off) const { return (T*)(p->ws + off); }
; __device__ __forceinline__ void ph_prep(Ctx& c, int gtid, int gthreads, int bid, int G, float* lds) {
;     ...
;         for (int k0 = kq * 256; k0 < kq * 256 + 256; k0 += 32) {
;             float w[32];
; #pragma unroll
;             for (int i = 0; i < 32; ++i) w[i] = aw[(size_t)(k0 + i) * 6144];
; #pragma unroll
;             for (int i = 0; i < 32; ++i)
; #pragma unroll
;                 for (int r = 0; r < 5; ++r) acc[r] = fmaf(lds[r * D + k0 + i], w[i], acc[r]);
;         }
; #pragma unroll
;         for (int r = 0; r < 5; ++r) lds[5 * D + (kq * 64 + jj) * 5 + r] = acc[r];
	v_mov_b32_e32 v136, v16
	s_waitcnt lgkmcnt(0)
	v_mov_b32_e32 v137, v158
	v_mov_b32_e32 v158, v17
	ds_read2_b32 v[16:17], v43 offset0:29 offset1:30
	v_pk_fma_f32 v[12:13], v[136:137], v[172:173], v[12:13] op_sel_hi:[1,0,1]
	s_waitcnt lgkmcnt(0)
	v_mov_b32_e32 v14, v16
	v_pk_fma_f32 v[12:13], v[158:159], v[174:175], v[12:13] op_sel_hi:[1,0,1]
	s_nop 0
	v_pk_fma_f32 v[12:13], v[14:15], v[176:177], v[12:13] op_sel_hi:[1,0,1]
	ds_read_b64 v[14:15], v43 offset:4216
	s_waitcnt lgkmcnt(0)
	v_pk_mov_b32 v[16:17], v[16:17], v[14:15] op_sel:[1,0]
	s_nop 0
	v_pk_fma_f32 v[12:13], v[16:17], v[178:179], v[12:13] op_sel_hi:[1,0,1]
	v_mov_b32_e32 v5, v15
	s_waitcnt vmcnt(32)
	v_pk_fma_f32 v[16:17], v[4:5], v[180:181], v[12:13] op_sel_hi:[1,0,1]
	ds_read_b32 v4, v43 offset:8316
	ds_read2_b32 v[12:13], v138 offset1:1
	s_waitcnt lgkmcnt(0)
	v_mov_b32_e32 v9, v12
	v_pk_fma_f32 v[8:9], v[8:9], v[160:161], v[18:19] op_sel_hi:[1,0,1]
	v_mov_b32_e32 v12, v10
	v_pk_fma_f32 v[8:9], v[12:13], v[162:163], v[8:9] op_sel_hi:[1,0,1]
	ds_read2_b32 v[12:13], v139 offset1:1
	ds_read2_b32 v[14:15], v140 offset1:1
	s_waitcnt lgkmcnt(1)
	v_mov_b32_e32 v18, v12
	s_waitcnt lgkmcnt(0)
	v_mov_b32_e32 v19, v14
	v_pk_fma_f32 v[8:9], v[18:19], v[164:165], v[8:9] op_sel_hi:[1,0,1]
	v_mov_b32_e32 v14, v13
	v_pk_fma_f32 v[8:9], v[14:15], v[166:167], v[8:9] op_sel_hi:[1,0,1]
	ds_read2_b32 v[12:13], v142 offset1:1
	ds_read2_b32 v[14:15], v143 offset1:1
	s_waitcnt lgkmcnt(1)
	v_mov_b32_e32 v18, v12
	s_waitcnt lgkmcnt(0)
	v_mov_b32_e32 v19, v14
	v_pk_fma_f32 v[8:9], v[18:19], v[168:169], v[8:9] op_sel_hi:[1,0,1]
	v_mov_b32_e32 v14, v13
	v_pk_fma_f32 v[8:9], v[14:15], v[170:171], v[8:9] op_sel_hi:[1,0,1]
	ds_read2_b32 v[12:13], v129 offset1:1
	ds_read2_b32 v[14:15], v130 offset1:1
	v_fmac_f32_e32 v41, v7, v180
	s_waitcnt lgkmcnt(1)
	v_mov_b32_e32 v18, v12
	s_waitcnt lgkmcnt(0)
	v_mov_b32_e32 v19, v14
	v_mov_b32_e32 v14, v13
	ds_read2_b32 v[12:13], v131 offset1:1
	v_pk_fma_f32 v[8:9], v[18:19], v[172:173], v[8:9] op_sel_hi:[1,0,1]
	s_waitcnt lgkmcnt(0)
	v_mov_b32_e32 v10, v12
	v_pk_fma_f32 v[8:9], v[14:15], v[174:175], v[8:9] op_sel_hi:[1,0,1]
	s_nop 0
	v_pk_fma_f32 v[8:9], v[10:11], v[176:177], v[8:9] op_sel_hi:[1,0,1]
	ds_read_b64 v[10:11], v43 offset:12408
	v_add_u32_e32 v45, 32, v45
	v_add_u32_e32 v43, 0x80, v43
	s_waitcnt lgkmcnt(0)
	v_pk_mov_b32 v[12:13], v[12:13], v[10:11] op_sel:[1,0]
	v_mov_b32_e32 v5, v11
	v_pk_fma_f32 v[8:9], v[12:13], v[178:179], v[8:9] op_sel_hi:[1,0,1]
	s_nop 0
	v_pk_fma_f32 v[18:19], v[4:5], v[180:181], v[8:9] op_sel_hi:[1,0,1]
	s_add_i32 s98, s98, 1
	s_branch .LBB0_602
.Lmod_last:
	v_add_u32_e32 v159, 0x304c, v43
	ds_read_b128 v[4:7], v43 offset:16384
	ds_read_b128 v[12:15], v43 offset:16416
	s_waitcnt vmcnt(31) lgkmcnt(1)
	v_fmac_f32_e32 v41, v4, v104
	s_waitcnt vmcnt(30)
	v_fmac_f32_e32 v41, v5, v106
	s_waitcnt vmcnt(29)
	v_fmac_f32_e32 v41, v6, v108
	s_waitcnt vmcnt(28)
	v_fmac_f32_e32 v41, v7, v110
	ds_read_b128 v[4:7], v43 offset:16400
	s_waitcnt vmcnt(27) lgkmcnt(0)
	v_fmac_f32_e32 v41, v4, v112
	s_waitcnt vmcnt(26)
	v_fmac_f32_e32 v41, v5, v114
	s_waitcnt vmcnt(25)
	v_fmac_f32_e32 v41, v6, v116
	s_waitcnt vmcnt(24)
	v_fmac_f32_e32 v41, v7, v118
	ds_read_b128 v[90:93], v43
	ds_read_b128 v[94:97], v43 offset:16
	ds_read_b128 v[8:11], v43 offset:32
	ds_read_b128 v[4:7], v43 offset:48
	ds_read_b128 v[98:101], v43 offset:4096
	s_waitcnt lgkmcnt(4)
	v_mov_b32_e32 v102, v90
	v_mov_b32_e32 v90, v92
	s_waitcnt vmcnt(23)
	v_fmac_f32_e32 v41, v12, v120
	s_waitcnt vmcnt(22)
	v_fmac_f32_e32 v41, v13, v122
	s_waitcnt lgkmcnt(0)
	v_mov_b32_e32 v103, v98
	v_pk_fma_f32 v[16:17], v[102:103], v[104:105], v[16:17] op_sel_hi:[1,0,1]
	v_mov_b32_e32 v98, v91
	v_pk_fma_f32 v[16:17], v[98:99], v[106:107], v[16:17] op_sel_hi:[1,0,1]
	v_mov_b32_e32 v91, v100
	v_pk_fma_f32 v[16:17], v[90:91], v[108:109], v[16:17] op_sel_hi:[1,0,1]
	v_mov_b32_e32 v100, v93
	ds_read_b128 v[90:93], v43 offset:4112
	v_pk_fma_f32 v[16:17], v[100:101], v[110:111], v[16:17] op_sel_hi:[1,0,1]
	v_mov_b32_e32 v98, v94
	v_mov_b32_e32 v94, v8
	s_waitcnt vmcnt(21)
	v_fmac_f32_e32 v41, v14, v124
	s_waitcnt lgkmcnt(0)
	v_mov_b32_e32 v99, v90
	v_pk_fma_f32 v[16:17], v[98:99], v[112:113], v[16:17] op_sel_hi:[1,0,1]
	v_mov_b32_e32 v90, v95
	v_pk_fma_f32 v[16:17], v[90:91], v[114:115], v[16:17] op_sel_hi:[1,0,1]
	v_mov_b32_e32 v90, v96
	v_mov_b32_e32 v91, v92
	v_pk_fma_f32 v[16:17], v[90:91], v[116:117], v[16:17] op_sel_hi:[1,0,1]
	v_mov_b32_e32 v92, v97
	v_pk_fma_f32 v[16:17], v[92:93], v[118:119], v[16:17] op_sel_hi:[1,0,1]
	ds_read_b128 v[90:93], v43 offset:4128
	s_waitcnt vmcnt(20)
	v_fmac_f32_e32 v41, v15, v126
	s_waitcnt lgkmcnt(0)
	v_mov_b32_e32 v95, v90
	v_pk_fma_f32 v[16:17], v[94:95], v[120:121], v[16:17] op_sel_hi:[1,0,1]
	ds_read_b128 v[94:97], v43 offset:8192
	ds_read_b128 v[98:101], v43 offset:12288
	v_mov_b32_e32 v90, v9
	v_pk_fma_f32 v[8:9], v[90:91], v[122:123], v[16:17] op_sel_hi:[1,0,1]
	s_waitcnt lgkmcnt(1)
	v_mov_b32_e32 v16, v94
	s_waitcnt lgkmcnt(0)
	v_mov_b32_e32 v17, v98
	v_pk_fma_f32 v[16:17], v[16:17], v[104:105], v[18:19] op_sel_hi:[1,0,1]
	v_mov_b32_e32 v98, v95
	v_pk_fma_f32 v[16:17], v[98:99], v[106:107], v[16:17] op_sel_hi:[1,0,1]
	v_mov_b32_e32 v18, v96
	v_mov_b32_e32 v19, v100
	v_pk_fma_f32 v[16:17], v[18:19], v[108:109], v[16:17] op_sel_hi:[1,0,1]
	v_mov_b32_e32 v100, v97
	v_pk_fma_f32 v[108:109], v[100:101], v[110:111], v[16:17] op_sel_hi:[1,0,1]
	ds_read_b128 v[16:19], v43 offset:8208
	ds_read_b128 v[104:107], v43 offset:12304
	s_waitcnt lgkmcnt(1)
	v_mov_b32_e32 v110, v16
	s_waitcnt lgkmcnt(0)
;     template <class T> __device__ __forceinline__ T* w(size_t off) const { return (T*)(p->ws + off); }
; __device__ __forceinline__ void ph_prep(Ctx& c, int gtid, int gthreads, int bid, int G, float* lds) {
;     ...
;             for (int i = 0; i < 32; ++i)
; #pragma unroll
;                 for (int r = 0; r < 5; ++r) acc[r] = fmaf(lds[r * D + k0 + i], w[i], acc[r]);
	v_mov_b32_e32 v111, v104
	v_pk_fma_f32 v[112:113], v[110:111], v[112:113], v[108:109] op_sel_hi:[1,0,1]
	v_mov_b32_e32 v104, v17
	v_pk_fma_f32 v[16:17], v[104:105], v[114:115], v[112:113] op_sel_hi:[1,0,1]
	v_mov_b32_e32 v112, v18
	v_mov_b32_e32 v113, v106
	v_pk_fma_f32 v[16:17], v[112:113], v[116:117], v[16:17] op_sel_hi:[1,0,1]
	v_mov_b32_e32 v106, v19
	v_pk_fma_f32 v[16:17], v[106:107], v[118:119], v[16:17] op_sel_hi:[1,0,1]
	ds_read_b128 v[112:115], v43 offset:8224
	ds_read_b128 v[116:119], v43 offset:12320
	ds_read_b128 v[12:15], v43 offset:16432
	v_mov_b32_e32 v104, v4
	s_waitcnt lgkmcnt(2)
	v_mov_b32_e32 v18, v112
	s_waitcnt lgkmcnt(1)
	v_mov_b32_e32 v19, v116
	v_pk_fma_f32 v[16:17], v[18:19], v[120:121], v[16:17] op_sel_hi:[1,0,1]
	v_mov_b32_e32 v116, v113
	s_waitcnt vmcnt(19) lgkmcnt(0)
	v_fmac_f32_e32 v41, v12, v128
	v_pk_fma_f32 v[112:113], v[116:117], v[122:123], v[16:17] op_sel_hi:[1,0,1]
	s_waitcnt vmcnt(18)
	v_fmac_f32_e32 v41, v13, v130
	v_mov_b32_e32 v116, v10
	v_mov_b32_e32 v117, v92
	s_waitcnt vmcnt(17)
	v_fmac_f32_e32 v41, v14, v132
	v_pk_fma_f32 v[8:9], v[116:117], v[124:125], v[8:9] op_sel_hi:[1,0,1]
	v_mov_b32_e32 v92, v11
	s_waitcnt vmcnt(16)
	v_fmac_f32_e32 v41, v15, v134
	ds_read_b128 v[12:15], v43 offset:16448
	ds_read_b96 v[120:122], v43 offset:4160
	ds_read_b96 v[16:18], v43 offset:12352
	v_pk_fma_f32 v[116:117], v[92:93], v[126:127], v[8:9] op_sel_hi:[1,0,1]
	ds_read_b128 v[8:11], v43 offset:4144
	v_add_u32_e32 v19, 0x104c, v43
	s_waitcnt vmcnt(15) lgkmcnt(3)
	v_fmac_f32_e32 v41, v12, v136
	s_waitcnt vmcnt(14)
	v_fmac_f32_e32 v41, v13, v138
	s_waitcnt vmcnt(13)
	v_fmac_f32_e32 v41, v14, v140
	s_waitcnt lgkmcnt(0)
	v_mov_b32_e32 v105, v8
	v_pk_fma_f32 v[116:117], v[104:105], v[128:129], v[116:117] op_sel_hi:[1,0,1]
	v_mov_b32_e32 v8, v5
	v_pk_fma_f32 v[4:5], v[8:9], v[130:131], v[116:117] op_sel_hi:[1,0,1]
	v_mov_b32_e32 v8, v6
	v_mov_b32_e32 v9, v10
	v_pk_fma_f32 v[4:5], v[8:9], v[132:133], v[4:5] op_sel_hi:[1,0,1]
	v_mov_b32_e32 v10, v7
	v_pk_fma_f32 v[8:9], v[10:11], v[134:135], v[4:5] op_sel_hi:[1,0,1]
	ds_read_b128 v[4:7], v43 offset:64
	v_mov_b32_e32 v11, v120
	ds_read_b96 v[12:14], v43 offset:80
	s_waitcnt vmcnt(12)
	v_fmac_f32_e32 v41, v15, v142
	s_waitcnt lgkmcnt(1)
	v_mov_b32_e32 v10, v4
	v_pk_fma_f32 v[8:9], v[10:11], v[136:137], v[8:9] op_sel_hi:[1,0,1]
	v_mov_b32_e32 v120, v5
	v_pk_fma_f32 v[4:5], v[120:121], v[138:139], v[8:9] op_sel_hi:[1,0,1]
	v_mov_b32_e32 v8, v6
	v_mov_b32_e32 v9, v122
	v_pk_fma_f32 v[4:5], v[8:9], v[140:141], v[4:5] op_sel_hi:[1,0,1]
	ds_read2_b32 v[8:9], v19 offset1:1
	s_waitcnt lgkmcnt(0)
	v_pk_mov_b32 v[6:7], v[6:7], v[8:9] op_sel:[1,0]
	s_nop 0
	v_pk_fma_f32 v[4:5], v[6:7], v[142:143], v[4:5] op_sel_hi:[1,0,1]
	v_mov_b32_e32 v8, v12
	s_waitcnt vmcnt(11)
	v_pk_fma_f32 v[120:121], v[8:9], v[158:159], v[4:5] op_sel_hi:[1,0,1]
	v_mov_b32_e32 v4, v114
	v_mov_b32_e32 v5, v118
	v_pk_fma_f32 v[4:5], v[4:5], v[124:125], v[112:113] op_sel_hi:[1,0,1]
	v_mov_b32_e32 v118, v115
	ds_read_b96 v[8:10], v43 offset:8272
	v_pk_fma_f32 v[122:123], v[118:119], v[126:127], v[4:5] op_sel_hi:[1,0,1]
	ds_read_b128 v[4:7], v43 offset:8240
	ds_read_b128 v[124:127], v43 offset:12336
	ds_read_b32 v11, v43 offset:12404
	ds_read_b32 v15, v43 offset:4212
	v_mov_b32_e32 v12, v13
	s_waitcnt lgkmcnt(3)
	v_mov_b32_e32 v112, v4
	s_waitcnt lgkmcnt(2)
	v_mov_b32_e32 v113, v124
	v_pk_fma_f32 v[128:129], v[112:113], v[128:129], v[122:123] op_sel_hi:[1,0,1]
	v_mov_b32_e32 v124, v5
	v_pk_fma_f32 v[4:5], v[124:125], v[130:131], v[128:129] op_sel_hi:[1,0,1]
	v_mov_b32_e32 v128, v6
	v_mov_b32_e32 v129, v126
	v_pk_fma_f32 v[4:5], v[128:129], v[132:133], v[4:5] op_sel_hi:[1,0,1]
	v_mov_b32_e32 v126, v7
	v_pk_fma_f32 v[128:129], v[126:127], v[134:135], v[4:5] op_sel_hi:[1,0,1]
	ds_read_b128 v[4:7], v43 offset:8256
	v_mov_b32_e32 v131, v16
	s_waitcnt lgkmcnt(0)
	v_mov_b32_e32 v130, v4
	v_pk_fma_f32 v[136:137], v[130:131], v[136:137], v[128:129] op_sel_hi:[1,0,1]
	v_mov_b32_e32 v16, v5
	v_pk_fma_f32 v[4:5], v[16:17], v[138:139], v[136:137] op_sel_hi:[1,0,1]
	v_mov_b32_e32 v16, v6
	v_mov_b32_e32 v17, v18
	v_pk_fma_f32 v[4:5], v[16:17], v[140:141], v[4:5] op_sel_hi:[1,0,1]
	ds_read2_b32 v[16:17], v159 offset1:1
	v_add_u32_e32 v141, 0x1064, v43
	v_add_u32_e32 v128, 0x106c, v43
	v_add_u32_e32 v138, 0x3054, v43
	v_add_u32_e32 v139, 0x205c, v43
	s_waitcnt lgkmcnt(0)
	v_pk_mov_b32 v[6:7], v[6:7], v[16:17] op_sel:[1,0]
	v_mov_b32_e32 v16, v8
	v_pk_fma_f32 v[4:5], v[6:7], v[142:143], v[4:5] op_sel_hi:[1,0,1]
	v_add_u32_e32 v8, 0x1054, v43
	v_pk_fma_f32 v[18:19], v[16:17], v[158:159], v[4:5] op_sel_hi:[1,0,1]
	ds_read_b128 v[4:7], v43 offset:16464
	v_add_u32_e32 v140, 0x305c, v43
	v_add_u32_e32 v142, 0x2064, v43
	v_add_u32_e32 v143, 0x3064, v43
	v_add_u32_e32 v129, 0x206c, v43
	s_waitcnt lgkmcnt(0)
	v_fmac_f32_e32 v41, v4, v158
	s_waitcnt vmcnt(10)
	v_fmac_f32_e32 v41, v5, v160
	s_waitcnt vmcnt(9)
;     template <class T> __device__ __forceinline__ T* w(size_t off) const { return (T*)(p->ws + off); }
; __device__ __forceinline__ void ph_prep(Ctx& c, int gtid, int gthreads, int bid, int G, float* lds) {
;     ...
;                 for (int r = 0; r < 5; ++r) acc[r] = fmaf(lds[r * D + k0 + i], w[i], acc[r]);
;         }
; #pragma unroll
;         for (int r = 0; r < 5; ++r) lds[5 * D + (kq * 64 + jj) * 5 + r] = acc[r];
;         __syncthreads();
;         for (int idx = tid; idx < 320; idx += NTHR) { const int j2 = idx / 5, r = idx % 5;
;             const float s = lds[5 * D + j2 * 5 + r] + lds[5 * D + (64 + j2) * 5 + r] + lds[5 * D + (128 + j2) * 5 + r] + lds[5 * D + (192 + j2) * 5 + r];
;             MOD[(l * 5 + r) * 6144 + j0 + j2] = s + c.in(5)[l * 6144 + j0 + j2]; }
	v_fmac_f32_e32 v41, v6, v162
	s_waitcnt vmcnt(8)
	v_fmac_f32_e32 v41, v7, v164
	ds_read_b128 v[4:7], v43 offset:16480
	v_add_u32_e32 v158, 0x105c, v43
	v_add_u32_e32 v130, 0x306c, v43
	v_add_u32_e32 v131, 0x2074, v43
	s_waitcnt vmcnt(7) lgkmcnt(0)
	v_fmac_f32_e32 v41, v4, v166
	s_waitcnt vmcnt(6)
	v_fmac_f32_e32 v41, v5, v168
	s_waitcnt vmcnt(5)
	v_fmac_f32_e32 v41, v6, v170
	s_waitcnt vmcnt(4)
	v_fmac_f32_e32 v41, v7, v172
	ds_read_b128 v[4:7], v43 offset:16496
	s_waitcnt vmcnt(3) lgkmcnt(0)
	v_fmac_f32_e32 v41, v4, v174
	ds_read_b32 v4, v43 offset:124
	ds_read2_b32 v[16:17], v8 offset1:1
	s_waitcnt vmcnt(2)
	v_fmac_f32_e32 v41, v5, v176
	s_waitcnt vmcnt(1)
	v_fmac_f32_e32 v41, v6, v178
	v_mov_b32_e32 v8, v9
	s_waitcnt lgkmcnt(0)
	v_mov_b32_e32 v13, v16
	v_pk_fma_f32 v[12:13], v[12:13], v[160:161], v[120:121] op_sel_hi:[1,0,1]
	v_mov_b32_e32 v16, v14
	v_pk_fma_f32 v[12:13], v[16:17], v[162:163], v[12:13] op_sel_hi:[1,0,1]
	ds_read2_b32 v[16:17], v43 offset0:23 offset1:24
	ds_read2_b32 v[158:159], v158 offset1:1
	s_waitcnt lgkmcnt(1)
	v_mov_b32_e32 v136, v16
	s_waitcnt lgkmcnt(0)
	v_mov_b32_e32 v137, v158
	v_pk_fma_f32 v[12:13], v[136:137], v[164:165], v[12:13] op_sel_hi:[1,0,1]
	v_mov_b32_e32 v158, v17
	v_pk_fma_f32 v[12:13], v[158:159], v[166:167], v[12:13] op_sel_hi:[1,0,1]
	ds_read2_b32 v[16:17], v43 offset0:25 offset1:26
	ds_read2_b32 v[158:159], v141 offset1:1
	s_waitcnt lgkmcnt(1)
	v_mov_b32_e32 v136, v16
	s_waitcnt lgkmcnt(0)
	v_mov_b32_e32 v137, v158
	v_pk_fma_f32 v[12:13], v[136:137], v[168:169], v[12:13] op_sel_hi:[1,0,1]
	v_mov_b32_e32 v158, v17
	v_pk_fma_f32 v[12:13], v[158:159], v[170:171], v[12:13] op_sel_hi:[1,0,1]
	ds_read2_b32 v[16:17], v43 offset0:27 offset1:28
	ds_read2_b32 v[158:159], v128 offset1:1
	s_waitcnt lgkmcnt(1)
	v_mov_b32_e32 v136, v16
	s_waitcnt lgkmcnt(0)
	v_mov_b32_e32 v137, v158
	v_mov_b32_e32 v158, v17
	ds_read2_b32 v[16:17], v43 offset0:29 offset1:30
	v_pk_fma_f32 v[12:13], v[136:137], v[172:173], v[12:13] op_sel_hi:[1,0,1]
	s_waitcnt lgkmcnt(0)
	v_mov_b32_e32 v14, v16
	v_pk_fma_f32 v[12:13], v[158:159], v[174:175], v[12:13] op_sel_hi:[1,0,1]
	s_nop 0
	v_pk_fma_f32 v[12:13], v[14:15], v[176:177], v[12:13] op_sel_hi:[1,0,1]
	ds_read_b64 v[14:15], v43 offset:4216
	s_waitcnt lgkmcnt(0)
	v_pk_mov_b32 v[16:17], v[16:17], v[14:15] op_sel:[1,0]
	s_nop 0
	v_pk_fma_f32 v[12:13], v[16:17], v[178:179], v[12:13] op_sel_hi:[1,0,1]
	v_mov_b32_e32 v5, v15
	s_waitcnt vmcnt(0)
	v_pk_fma_f32 v[16:17], v[4:5], v[180:181], v[12:13] op_sel_hi:[1,0,1]
	ds_read_b32 v4, v43 offset:8316
	ds_read2_b32 v[12:13], v138 offset1:1
	s_waitcnt lgkmcnt(0)
	v_mov_b32_e32 v9, v12
	v_pk_fma_f32 v[8:9], v[8:9], v[160:161], v[18:19] op_sel_hi:[1,0,1]
	v_mov_b32_e32 v12, v10
	v_pk_fma_f32 v[8:9], v[12:13], v[162:163], v[8:9] op_sel_hi:[1,0,1]
	ds_read2_b32 v[12:13], v139 offset1:1
	ds_read2_b32 v[14:15], v140 offset1:1
	s_waitcnt lgkmcnt(1)
	v_mov_b32_e32 v18, v12
	s_waitcnt lgkmcnt(0)
	v_mov_b32_e32 v19, v14
	v_pk_fma_f32 v[8:9], v[18:19], v[164:165], v[8:9] op_sel_hi:[1,0,1]
	v_mov_b32_e32 v14, v13
	v_pk_fma_f32 v[8:9], v[14:15], v[166:167], v[8:9] op_sel_hi:[1,0,1]
	ds_read2_b32 v[12:13], v142 offset1:1
	ds_read2_b32 v[14:15], v143 offset1:1
	s_waitcnt lgkmcnt(1)
	v_mov_b32_e32 v18, v12
	s_waitcnt lgkmcnt(0)
	v_mov_b32_e32 v19, v14
	v_pk_fma_f32 v[8:9], v[18:19], v[168:169], v[8:9] op_sel_hi:[1,0,1]
	v_mov_b32_e32 v14, v13
	v_pk_fma_f32 v[8:9], v[14:15], v[170:171], v[8:9] op_sel_hi:[1,0,1]
	ds_read2_b32 v[12:13], v129 offset1:1
	ds_read2_b32 v[14:15], v130 offset1:1
	v_fmac_f32_e32 v41, v7, v180
	s_waitcnt lgkmcnt(1)
	v_mov_b32_e32 v18, v12
	s_waitcnt lgkmcnt(0)
	v_mov_b32_e32 v19, v14
	v_mov_b32_e32 v14, v13
	ds_read2_b32 v[12:13], v131 offset1:1
	v_pk_fma_f32 v[8:9], v[18:19], v[172:173], v[8:9] op_sel_hi:[1,0,1]
	s_waitcnt lgkmcnt(0)
	v_mov_b32_e32 v10, v12
	v_pk_fma_f32 v[8:9], v[14:15], v[174:175], v[8:9] op_sel_hi:[1,0,1]
	s_nop 0
	v_pk_fma_f32 v[8:9], v[10:11], v[176:177], v[8:9] op_sel_hi:[1,0,1]
	ds_read_b64 v[10:11], v43 offset:12408
	v_add_u32_e32 v45, 32, v45
	v_add_u32_e32 v43, 0x80, v43
	s_waitcnt lgkmcnt(0)
	v_pk_mov_b32 v[12:13], v[12:13], v[10:11] op_sel:[1,0]
	v_mov_b32_e32 v5, v11
	v_pk_fma_f32 v[8:9], v[12:13], v[178:179], v[8:9] op_sel_hi:[1,0,1]
	s_nop 0
	v_pk_fma_f32 v[18:19], v[4:5], v[180:181], v[8:9] op_sel_hi:[1,0,1]
	s_or_b64 exec, exec, s[48:49]
	v_add_u32_e32 v2, 0x5000, v31
	ds_write2_b32 v2, v16, v17 offset1:1
	v_add_u32_e32 v2, 0x5008, v31
	ds_write2_b32 v2, v18, v19 offset1:1
	ds_write_b32 v31, v41 offset:20496
	s_waitcnt lgkmcnt(0)
	s_barrier
	s_and_saveexec_b64 s[28:29], s[46:47]
	s_cbranch_execz .LBB0_593
	s_movk_i32 s16, 0x1800
	s_mul_i32 s7, s6, 0x1800
	s_mulk_i32 s6, 0x6000
	v_mul_lo_u32 v2, v156, s16
	s_lshl_b32 s16, s15, 6
	s_add_i32 s16, s16, s6
	s_add_i32 s7, s44, s7
	v_add_u32_e32 v2, s16, v2
	s_mov_b64 s[44:45], 0
	v_mov_b32_e32 v4, v39
	v_mov_b32_e32 v5, v156
